# P5/P8/P9 GEMM epilogue output stores made write-through (sc0 sc1) so the grid barrier's L2 writeback has less to flush
# speedup vs baseline: 1.0047x; 1.0012x over previous
; __device__ __forceinline__ unsigned cvt_pk_bf16(float lo, float hi) { unsigned r; asm volatile("v_cvt_pk_bf16_f32 %0, %1, %2" : "=v"(r) : "v"(lo), "v"(hi)); return r; }
;     __device__ __forceinline__ void operator()(const f32x4 (&acc)[2][2][4][2], const Unit& u, int wr, int wc, int fr, int fq) const {
;     ...
;                 const int row = row0 + ai * HALF + m * 16; const size_t off = (size_t)row * 1024 + col0; float s = 0.f;
; #pragma unroll
;                 for (int bj = 0; bj < 2; ++bj) { const size_t o2 = off + bj * HALF;
;                     f32x4 b0, b1;
;                     if (BASE_F32) { b0 = *(const f32x4*)(basef + o2); b1 = *(const f32x4*)(basef + o2 + 4); }
;                     else { const u32x4 p = *(const u32x4*)(xb + o2);
;                         b0 = (f32x4){__builtin_bit_cast(float, p.x << 16), __builtin_bit_cast(float, p.x & 0xffff0000u), __builtin_bit_cast(float, p.y << 16), __builtin_bit_cast(float, p.y & 0xffff0000u)};
;                         b1 = (f32x4){__builtin_bit_cast(float, p.z << 16), __builtin_bit_cast(float, p.z & 0xffff0000u), __builtin_bit_cast(float, p.w << 16), __builtin_bit_cast(float, p.w & 0xffff0000u)}; }
;                     const f32x4 o0 = b0 + acc[ai][bj][m][0], o1 = b1 + acc[ai][bj][m][1];
;                     s += ((o0[0] * o0[0] + o0[1] * o0[1]) + (o0[2] * o0[2] + o0[3] * o0[3])) + ((o1[0] * o1[0] + o1[1] * o1[1]) + (o1[2] * o1[2] + o1[3] * o1[3]));
;                     u32x4 w; w.x = cvt_pk_bf16(o0[0], o0[1]); w.y = cvt_pk_bf16(o0[2], o0[3]); w.z = cvt_pk_bf16(o1[0], o1[1]); w.w = cvt_pk_bf16(o1[2], o1[3]);
;                     *(u32x4*)(xb + o2) = w; }
;                 s += __shfl_xor(s, 16); s += __shfl_xor(s, 32);
;                 if (fq == 0) atomicAdd(ssq + row, s);
.LBB0_2351:
	v_lshl_add_u32 v148, s40, 8, v1
	v_lshl_or_b32 v146, s42, 8, v151
	v_ashrrev_i32_e32 v149, 31, v148
	v_readlane_b32 s56, v254, 4
	v_ashrrev_i32_e32 v147, 31, v146
	v_lshlrev_b64 v[156:157], 10, v[148:149]
	v_readlane_b32 s57, v254, 5
	v_lshl_add_u64 v[164:165], v[156:157], 0, v[146:147]
	s_mov_b64 s[36:37], s[56:57]
	v_lshl_add_u64 v[166:167], v[164:165], 2, s[36:37]
	global_load_dwordx4 v[156:159], v[166:167], off
	global_load_dwordx4 v[160:163], v[166:167], off offset:16
	v_lshlrev_b64 v[164:165], 1, v[164:165]
	v_lshl_add_u64 v[168:169], s[80:81], 0, v[164:165]
	v_or_b32_e32 v164, 0x100, v164
	v_readlane_b32 s58, v254, 6
	v_readlane_b32 s59, v254, 7
	v_readlane_b32 s60, v254, 8
	v_readlane_b32 s61, v254, 9
	v_readlane_b32 s62, v254, 10
	v_readlane_b32 s63, v254, 11
	v_readlane_b32 s64, v254, 12
	v_readlane_b32 s65, v254, 13
	v_readlane_b32 s66, v254, 14
	v_readlane_b32 s67, v254, 15
	v_readlane_b32 s68, v254, 16
	v_readlane_b32 s69, v254, 17
	v_readlane_b32 s70, v254, 18
	v_readlane_b32 s71, v254, 19
	s_waitcnt vmcnt(0)
	v_pk_add_f32 v[128:129], v[128:129], v[158:159]
	v_pk_add_f32 v[170:171], v[126:127], v[156:157]
	v_pk_add_f32 v[162:163], v[124:125], v[162:163]
	v_pk_add_f32 v[160:161], v[122:123], v[160:161]
	v_cvt_pk_bf16_f32 v122, v170, v171
	v_cvt_pk_bf16_f32 v123, v128, v129
	v_mul_f32_e32 v129, v129, v129
	v_cvt_pk_bf16_f32 v124, v160, v161
	v_cvt_pk_bf16_f32 v125, v162, v163
	global_store_dwordx4 v[168:169], v[122:125], off sc0 sc1
	global_load_dwordx4 v[124:127], v[166:167], off offset:512
	s_nop 0
	global_load_dwordx4 v[156:159], v[166:167], off offset:528
	v_and_b32_e32 v123, 64, v155
	v_mul_f32_e32 v167, v171, v171
	v_mul_f32_e32 v161, v161, v161
	v_mul_f32_e32 v163, v163, v163
	v_xor_b32_e32 v122, 16, v155
	v_add_u32_e32 v123, 64, v123
	v_fmac_f32_e32 v167, v170, v170
	v_fmac_f32_e32 v129, v128, v128
	v_fmac_f32_e32 v161, v160, v160
	v_fmac_f32_e32 v163, v162, v162
	v_cmp_lt_i32_e32 vcc, v122, v123
	v_add_f32_e32 v128, v167, v129
	v_add_f32_e32 v129, v161, v163
	v_cndmask_b32_e32 v122, v155, v122, vcc
	v_add_f32_e32 v128, v128, v129
	v_lshlrev_b32_e32 v122, 2, v122
	v_xor_b32_e32 v166, 32, v155
	v_cmp_lt_i32_e32 vcc, v166, v123
	s_waitcnt vmcnt(1)
	v_pk_add_f32 v[120:121], v[120:121], v[126:127]
	v_pk_add_f32 v[118:119], v[118:119], v[124:125]
	s_waitcnt vmcnt(0)
	v_pk_add_f32 v[124:125], v[116:117], v[158:159]
	v_pk_add_f32 v[114:115], v[114:115], v[156:157]
	v_mul_f32_e32 v116, v119, v119
	v_mul_f32_e32 v117, v121, v121
	v_mul_f32_e32 v126, v115, v115
	v_mul_f32_e32 v127, v125, v125
	v_fmac_f32_e32 v116, v118, v118
	v_fmac_f32_e32 v117, v120, v120
	v_fmac_f32_e32 v126, v114, v114
	v_fmac_f32_e32 v127, v124, v124
	v_add_f32_e32 v116, v116, v117
	v_add_f32_e32 v117, v126, v127
	v_add_f32_e32 v116, v116, v117
	v_add_f32_e32 v116, v128, v116
	ds_bpermute_b32 v117, v122, v116
	v_cndmask_b32_e32 v123, v155, v166, vcc
	v_cvt_pk_bf16_f32 v118, v118, v119
	v_cvt_pk_bf16_f32 v119, v120, v121
	v_cvt_pk_bf16_f32 v120, v114, v115
	s_waitcnt lgkmcnt(0)
	v_add_f32_e32 v114, v116, v117
	v_lshlrev_b32_e32 v116, 2, v123
	ds_bpermute_b32 v115, v116, v114
	v_cvt_pk_bf16_f32 v121, v124, v125
	v_lshl_add_u64 v[124:125], s[80:81], 0, v[164:165]
	global_store_dwordx4 v[124:125], v[118:121], off sc0 sc1
	s_and_saveexec_b64 s[22:23], s[4:5]
	s_cbranch_execz .LBB0_2353
	v_lshl_add_u64 v[118:119], v[148:149], 2, s[10:11]
	s_waitcnt lgkmcnt(0)
	v_add_f32_e32 v114, v114, v115
	global_atomic_add_f32 v[118:119], v114, off
.LBB0_2353:
	s_or_b64 exec, exec, s[22:23]
	v_or_b32_e32 v114, 16, v148
	s_waitcnt lgkmcnt(0)
	v_ashrrev_i32_e32 v115, 31, v114
	v_lshlrev_b64 v[118:119], 10, v[114:115]
	v_lshl_add_u64 v[128:129], v[118:119], 0, v[146:147]
	v_lshl_add_u64 v[156:157], v[128:129], 2, s[36:37]
	global_load_dwordx4 v[118:121], v[156:157], off
	global_load_dwordx4 v[124:127], v[156:157], off offset:16
	v_lshlrev_b64 v[128:129], 1, v[128:129]
	v_lshl_add_u64 v[158:159], s[80:81], 0, v[128:129]
	v_or_b32_e32 v128, 0x100, v128
	s_waitcnt vmcnt(1)
	v_pk_add_f32 v[120:121], v[112:113], v[120:121]
	v_pk_add_f32 v[118:119], v[110:111], v[118:119]
	s_waitcnt vmcnt(0)
	v_pk_add_f32 v[126:127], v[108:109], v[126:127]
	v_pk_add_f32 v[124:125], v[106:107], v[124:125]
	v_cvt_pk_bf16_f32 v106, v118, v119
	v_cvt_pk_bf16_f32 v107, v120, v121
	v_mul_f32_e32 v117, v119, v119
	v_cvt_pk_bf16_f32 v108, v124, v125
	v_cvt_pk_bf16_f32 v109, v126, v127
	global_store_dwordx4 v[158:159], v[106:109], off sc0 sc1
	global_load_dwordx4 v[106:109], v[156:157], off offset:512
	s_nop 0
	global_load_dwordx4 v[110:113], v[156:157], off offset:528
	v_mul_f32_e32 v119, v121, v121
	v_mul_f32_e32 v121, v125, v125
	v_mul_f32_e32 v123, v127, v127
	v_fmac_f32_e32 v117, v118, v118
	v_fmac_f32_e32 v119, v120, v120
	v_fmac_f32_e32 v121, v124, v124
	v_fmac_f32_e32 v123, v126, v126
	v_add_f32_e32 v117, v117, v119
	v_add_f32_e32 v118, v121, v123
	v_add_f32_e32 v117, v117, v118
	s_waitcnt vmcnt(1)
	v_pk_add_f32 v[104:105], v[104:105], v[108:109]
	v_pk_add_f32 v[102:103], v[102:103], v[106:107]
	s_waitcnt vmcnt(0)
	v_pk_add_f32 v[106:107], v[100:101], v[112:113]
	v_pk_add_f32 v[98:99], v[98:99], v[110:111]
	v_mul_f32_e32 v100, v103, v103
	v_mul_f32_e32 v101, v105, v105
	v_mul_f32_e32 v108, v99, v99
	v_mul_f32_e32 v109, v107, v107
	v_fmac_f32_e32 v100, v102, v102
	v_fmac_f32_e32 v101, v104, v104
	v_fmac_f32_e32 v108, v98, v98
	v_fmac_f32_e32 v109, v106, v106
	v_add_f32_e32 v100, v100, v101
	v_add_f32_e32 v101, v108, v109
	v_add_f32_e32 v100, v100, v101
	v_add_f32_e32 v108, v117, v100
	ds_bpermute_b32 v109, v122, v108
	v_cvt_pk_bf16_f32 v100, v102, v103
	v_cvt_pk_bf16_f32 v101, v104, v105
	v_cvt_pk_bf16_f32 v102, v98, v99
	v_lshl_add_u64 v[104:105], s[80:81], 0, v[128:129]
	s_waitcnt lgkmcnt(0)
	v_add_f32_e32 v98, v108, v109
	ds_bpermute_b32 v99, v116, v98
	v_cvt_pk_bf16_f32 v103, v106, v107
	global_store_dwordx4 v[104:105], v[100:103], off sc0 sc1
	s_and_saveexec_b64 s[22:23], s[4:5]
	s_cbranch_execz .LBB0_2355
	v_lshl_add_u64 v[100:101], v[114:115], 2, s[10:11]
	s_waitcnt lgkmcnt(0)
	v_add_f32_e32 v98, v98, v99
	global_atomic_add_f32 v[100:101], v98, off
; __device__ __forceinline__ unsigned cvt_pk_bf16(float lo, float hi) { unsigned r; asm volatile("v_cvt_pk_bf16_f32 %0, %1, %2" : "=v"(r) : "v"(lo), "v"(hi)); return r; }
;     __device__ __forceinline__ void operator()(const f32x4 (&acc)[2][2][4][2], const Unit& u, int wr, int wc, int fr, int fq) const {
;     ...
;                 const int row = row0 + ai * HALF + m * 16; const size_t off = (size_t)row * 1024 + col0; float s = 0.f;
; #pragma unroll
;                 for (int bj = 0; bj < 2; ++bj) { const size_t o2 = off + bj * HALF;
;                     f32x4 b0, b1;
;                     if (BASE_F32) { b0 = *(const f32x4*)(basef + o2); b1 = *(const f32x4*)(basef + o2 + 4); }
;                     else { const u32x4 p = *(const u32x4*)(xb + o2);
;                         b0 = (f32x4){__builtin_bit_cast(float, p.x << 16), __builtin_bit_cast(float, p.x & 0xffff0000u), __builtin_bit_cast(float, p.y << 16), __builtin_bit_cast(float, p.y & 0xffff0000u)};
;                         b1 = (f32x4){__builtin_bit_cast(float, p.z << 16), __builtin_bit_cast(float, p.z & 0xffff0000u), __builtin_bit_cast(float, p.w << 16), __builtin_bit_cast(float, p.w & 0xffff0000u)}; }
;                     const f32x4 o0 = b0 + acc[ai][bj][m][0], o1 = b1 + acc[ai][bj][m][1];
;                     s += ((o0[0] * o0[0] + o0[1] * o0[1]) + (o0[2] * o0[2] + o0[3] * o0[3])) + ((o1[0] * o1[0] + o1[1] * o1[1]) + (o1[2] * o1[2] + o1[3] * o1[3]));
;                     u32x4 w; w.x = cvt_pk_bf16(o0[0], o0[1]); w.y = cvt_pk_bf16(o0[2], o0[3]); w.z = cvt_pk_bf16(o1[0], o1[1]); w.w = cvt_pk_bf16(o1[2], o1[3]);
;                     *(u32x4*)(xb + o2) = w; }
;                 s += __shfl_xor(s, 16); s += __shfl_xor(s, 32);
;                 if (fq == 0) atomicAdd(ssq + row, s);
.LBB0_2355:
	s_or_b64 exec, exec, s[22:23]
	v_or_b32_e32 v98, 32, v148
	s_waitcnt lgkmcnt(0)
	v_ashrrev_i32_e32 v99, 31, v98
	v_lshlrev_b64 v[100:101], 10, v[98:99]
	v_lshl_add_u64 v[108:109], v[100:101], 0, v[146:147]
	v_lshl_add_u64 v[110:111], v[108:109], 2, s[36:37]
	global_load_dwordx4 v[100:103], v[110:111], off
	global_load_dwordx4 v[104:107], v[110:111], off offset:16
	v_lshlrev_b64 v[108:109], 1, v[108:109]
	v_lshl_add_u64 v[112:113], s[80:81], 0, v[108:109]
	v_or_b32_e32 v108, 0x100, v108
	s_waitcnt vmcnt(1)
	v_pk_add_f32 v[102:103], v[96:97], v[102:103]
	v_pk_add_f32 v[100:101], v[94:95], v[100:101]
	s_waitcnt vmcnt(0)
	v_pk_add_f32 v[106:107], v[92:93], v[106:107]
	v_pk_add_f32 v[104:105], v[90:91], v[104:105]
	v_cvt_pk_bf16_f32 v90, v100, v101
	v_cvt_pk_bf16_f32 v91, v102, v103
	v_mul_f32_e32 v101, v101, v101
	v_cvt_pk_bf16_f32 v92, v104, v105
	v_cvt_pk_bf16_f32 v93, v106, v107
	global_store_dwordx4 v[112:113], v[90:93], off sc0 sc1
	global_load_dwordx4 v[90:93], v[110:111], off offset:512
	s_nop 0
	global_load_dwordx4 v[94:97], v[110:111], off offset:528
	v_mul_f32_e32 v103, v103, v103
	v_mul_f32_e32 v105, v105, v105
	v_mul_f32_e32 v107, v107, v107
	v_fmac_f32_e32 v101, v100, v100
	v_fmac_f32_e32 v103, v102, v102
	v_fmac_f32_e32 v105, v104, v104
	v_fmac_f32_e32 v107, v106, v106
	v_add_f32_e32 v100, v101, v103
	v_add_f32_e32 v101, v105, v107
	v_add_f32_e32 v100, v100, v101
	s_waitcnt vmcnt(1)
	v_pk_add_f32 v[88:89], v[88:89], v[92:93]
	v_pk_add_f32 v[86:87], v[86:87], v[90:91]
	s_waitcnt vmcnt(0)
	v_pk_add_f32 v[90:91], v[84:85], v[96:97]
	v_pk_add_f32 v[82:83], v[82:83], v[94:95]
	v_mul_f32_e32 v84, v87, v87
	v_mul_f32_e32 v85, v89, v89
	v_mul_f32_e32 v92, v83, v83
	v_mul_f32_e32 v93, v91, v91
	v_fmac_f32_e32 v84, v86, v86
	v_fmac_f32_e32 v85, v88, v88
	v_fmac_f32_e32 v92, v82, v82
	v_fmac_f32_e32 v93, v90, v90
	v_add_f32_e32 v84, v84, v85
	v_add_f32_e32 v85, v92, v93
	v_add_f32_e32 v84, v84, v85
	v_add_f32_e32 v92, v100, v84
	ds_bpermute_b32 v93, v122, v92
	v_cvt_pk_bf16_f32 v84, v86, v87
	v_cvt_pk_bf16_f32 v85, v88, v89
	v_cvt_pk_bf16_f32 v86, v82, v83
	v_lshl_add_u64 v[88:89], s[80:81], 0, v[108:109]
	s_waitcnt lgkmcnt(0)
	v_add_f32_e32 v82, v92, v93
	ds_bpermute_b32 v83, v116, v82
	v_cvt_pk_bf16_f32 v87, v90, v91
	global_store_dwordx4 v[88:89], v[84:87], off sc0 sc1
	s_and_saveexec_b64 s[22:23], s[4:5]
	s_cbranch_execz .LBB0_2357
	v_lshl_add_u64 v[84:85], v[98:99], 2, s[10:11]
	s_waitcnt lgkmcnt(0)
	v_add_f32_e32 v82, v82, v83
	global_atomic_add_f32 v[84:85], v82, off
.LBB0_2357:
	s_or_b64 exec, exec, s[22:23]
	v_or_b32_e32 v82, 48, v148
	s_waitcnt lgkmcnt(0)
	v_ashrrev_i32_e32 v83, 31, v82
	v_lshlrev_b64 v[84:85], 10, v[82:83]
	v_lshl_add_u64 v[92:93], v[84:85], 0, v[146:147]
	v_lshl_add_u64 v[94:95], v[92:93], 2, s[36:37]
	global_load_dwordx4 v[84:87], v[94:95], off
	global_load_dwordx4 v[88:91], v[94:95], off offset:16
	v_lshlrev_b64 v[92:93], 1, v[92:93]
	v_lshl_add_u64 v[96:97], s[80:81], 0, v[92:93]
	v_or_b32_e32 v92, 0x100, v92
	s_waitcnt vmcnt(1)
	v_pk_add_f32 v[86:87], v[80:81], v[86:87]
	v_pk_add_f32 v[84:85], v[78:79], v[84:85]
	s_waitcnt vmcnt(0)
	v_pk_add_f32 v[90:91], v[76:77], v[90:91]
	v_pk_add_f32 v[88:89], v[74:75], v[88:89]
	v_cvt_pk_bf16_f32 v74, v84, v85
	v_cvt_pk_bf16_f32 v75, v86, v87
	v_mul_f32_e32 v85, v85, v85
	v_cvt_pk_bf16_f32 v76, v88, v89
	v_cvt_pk_bf16_f32 v77, v90, v91
	global_store_dwordx4 v[96:97], v[74:77], off sc0 sc1
	global_load_dwordx4 v[74:77], v[94:95], off offset:512
	s_nop 0
	global_load_dwordx4 v[78:81], v[94:95], off offset:528
	v_mul_f32_e32 v87, v87, v87
	v_mul_f32_e32 v89, v89, v89
	v_mul_f32_e32 v91, v91, v91
	v_fmac_f32_e32 v85, v84, v84
	v_fmac_f32_e32 v87, v86, v86
	v_fmac_f32_e32 v89, v88, v88
	v_fmac_f32_e32 v91, v90, v90
	v_add_f32_e32 v84, v85, v87
	v_add_f32_e32 v85, v89, v91
	v_add_f32_e32 v84, v84, v85
	s_waitcnt vmcnt(1)
	v_pk_add_f32 v[72:73], v[72:73], v[76:77]
	v_pk_add_f32 v[70:71], v[70:71], v[74:75]
	s_waitcnt vmcnt(0)
	v_pk_add_f32 v[74:75], v[68:69], v[80:81]
	v_pk_add_f32 v[66:67], v[66:67], v[78:79]
	v_mul_f32_e32 v68, v71, v71
	v_mul_f32_e32 v69, v73, v73
	v_mul_f32_e32 v76, v67, v67
	v_mul_f32_e32 v77, v75, v75
	v_fmac_f32_e32 v68, v70, v70
	v_fmac_f32_e32 v69, v72, v72
	v_fmac_f32_e32 v76, v66, v66
	v_fmac_f32_e32 v77, v74, v74
	v_add_f32_e32 v68, v68, v69
	v_add_f32_e32 v69, v76, v77
	v_add_f32_e32 v68, v68, v69
	v_add_f32_e32 v76, v84, v68
	ds_bpermute_b32 v77, v122, v76
	v_cvt_pk_bf16_f32 v68, v70, v71
	v_cvt_pk_bf16_f32 v69, v72, v73
	v_cvt_pk_bf16_f32 v70, v66, v67
	v_lshl_add_u64 v[72:73], s[80:81], 0, v[92:93]
	s_waitcnt lgkmcnt(0)
	v_add_f32_e32 v66, v76, v77
	ds_bpermute_b32 v67, v116, v66
	v_cvt_pk_bf16_f32 v71, v74, v75
	global_store_dwordx4 v[72:73], v[68:71], off sc0 sc1
	s_and_saveexec_b64 s[22:23], s[4:5]
	s_cbranch_execz .LBB0_2359
	v_lshl_add_u64 v[68:69], v[82:83], 2, s[10:11]
	s_waitcnt lgkmcnt(0)
	v_add_f32_e32 v66, v66, v67
	global_atomic_add_f32 v[68:69], v66, off
; __device__ __forceinline__ unsigned cvt_pk_bf16(float lo, float hi) { unsigned r; asm volatile("v_cvt_pk_bf16_f32 %0, %1, %2" : "=v"(r) : "v"(lo), "v"(hi)); return r; }
;     __device__ __forceinline__ void operator()(const f32x4 (&acc)[2][2][4][2], const Unit& u, int wr, int wc, int fr, int fq) const {
;     ...
;                 const int row = row0 + ai * HALF + m * 16; const size_t off = (size_t)row * 1024 + col0; float s = 0.f;
; #pragma unroll
;                 for (int bj = 0; bj < 2; ++bj) { const size_t o2 = off + bj * HALF;
;                     f32x4 b0, b1;
;                     if (BASE_F32) { b0 = *(const f32x4*)(basef + o2); b1 = *(const f32x4*)(basef + o2 + 4); }
;                     else { const u32x4 p = *(const u32x4*)(xb + o2);
;                         b0 = (f32x4){__builtin_bit_cast(float, p.x << 16), __builtin_bit_cast(float, p.x & 0xffff0000u), __builtin_bit_cast(float, p.y << 16), __builtin_bit_cast(float, p.y & 0xffff0000u)};
;                         b1 = (f32x4){__builtin_bit_cast(float, p.z << 16), __builtin_bit_cast(float, p.z & 0xffff0000u), __builtin_bit_cast(float, p.w << 16), __builtin_bit_cast(float, p.w & 0xffff0000u)}; }
;                     const f32x4 o0 = b0 + acc[ai][bj][m][0], o1 = b1 + acc[ai][bj][m][1];
;                     s += ((o0[0] * o0[0] + o0[1] * o0[1]) + (o0[2] * o0[2] + o0[3] * o0[3])) + ((o1[0] * o1[0] + o1[1] * o1[1]) + (o1[2] * o1[2] + o1[3] * o1[3]));
;                     u32x4 w; w.x = cvt_pk_bf16(o0[0], o0[1]); w.y = cvt_pk_bf16(o0[2], o0[3]); w.z = cvt_pk_bf16(o1[0], o1[1]); w.w = cvt_pk_bf16(o1[2], o1[3]);
;                     *(u32x4*)(xb + o2) = w; }
;                 s += __shfl_xor(s, 16); s += __shfl_xor(s, 32);
;                 if (fq == 0) atomicAdd(ssq + row, s);
.LBB0_2359:
	s_or_b64 exec, exec, s[22:23]
	v_add_u32_e32 v66, 0x80, v148
	s_waitcnt lgkmcnt(0)
	v_ashrrev_i32_e32 v67, 31, v66
	v_lshlrev_b64 v[68:69], 10, v[66:67]
	v_lshl_add_u64 v[76:77], v[68:69], 0, v[146:147]
	v_lshl_add_u64 v[78:79], v[76:77], 2, s[36:37]
	global_load_dwordx4 v[68:71], v[78:79], off
	global_load_dwordx4 v[72:75], v[78:79], off offset:16
	v_lshlrev_b64 v[76:77], 1, v[76:77]
	v_lshl_add_u64 v[80:81], s[80:81], 0, v[76:77]
	v_or_b32_e32 v76, 0x100, v76
	s_waitcnt vmcnt(1)
	v_pk_add_f32 v[70:71], v[64:65], v[70:71]
	v_pk_add_f32 v[68:69], v[62:63], v[68:69]
	s_waitcnt vmcnt(0)
	v_pk_add_f32 v[74:75], v[60:61], v[74:75]
	v_pk_add_f32 v[72:73], v[58:59], v[72:73]
	v_cvt_pk_bf16_f32 v58, v68, v69
	v_cvt_pk_bf16_f32 v59, v70, v71
	v_mul_f32_e32 v69, v69, v69
	v_cvt_pk_bf16_f32 v60, v72, v73
	v_cvt_pk_bf16_f32 v61, v74, v75
	global_store_dwordx4 v[80:81], v[58:61], off sc0 sc1
	global_load_dwordx4 v[58:61], v[78:79], off offset:512
	s_nop 0
	global_load_dwordx4 v[62:65], v[78:79], off offset:528
	v_mul_f32_e32 v71, v71, v71
	v_mul_f32_e32 v73, v73, v73
	v_mul_f32_e32 v75, v75, v75
	v_fmac_f32_e32 v69, v68, v68
	v_fmac_f32_e32 v71, v70, v70
	v_fmac_f32_e32 v73, v72, v72
	v_fmac_f32_e32 v75, v74, v74
	v_add_f32_e32 v68, v69, v71
	v_add_f32_e32 v69, v73, v75
	v_add_f32_e32 v68, v68, v69
	s_waitcnt vmcnt(1)
	v_pk_add_f32 v[56:57], v[56:57], v[60:61]
	v_pk_add_f32 v[54:55], v[54:55], v[58:59]
	s_waitcnt vmcnt(0)
	v_pk_add_f32 v[58:59], v[52:53], v[64:65]
	v_pk_add_f32 v[50:51], v[50:51], v[62:63]
	v_mul_f32_e32 v52, v55, v55
	v_mul_f32_e32 v53, v57, v57
	v_mul_f32_e32 v60, v51, v51
	v_mul_f32_e32 v61, v59, v59
	v_fmac_f32_e32 v52, v54, v54
	v_fmac_f32_e32 v53, v56, v56
	v_fmac_f32_e32 v60, v50, v50
	v_fmac_f32_e32 v61, v58, v58
	v_add_f32_e32 v52, v52, v53
	v_add_f32_e32 v53, v60, v61
	v_add_f32_e32 v52, v52, v53
	v_add_f32_e32 v60, v68, v52
	ds_bpermute_b32 v61, v122, v60
	v_cvt_pk_bf16_f32 v52, v54, v55
	v_cvt_pk_bf16_f32 v53, v56, v57
	v_cvt_pk_bf16_f32 v54, v50, v51
	v_lshl_add_u64 v[56:57], s[80:81], 0, v[76:77]
	s_waitcnt lgkmcnt(0)
	v_add_f32_e32 v50, v60, v61
	ds_bpermute_b32 v51, v116, v50
	v_cvt_pk_bf16_f32 v55, v58, v59
	global_store_dwordx4 v[56:57], v[52:55], off sc0 sc1
	s_and_saveexec_b64 s[22:23], s[4:5]
	s_cbranch_execz .LBB0_2361
	v_lshl_add_u64 v[52:53], v[66:67], 2, s[10:11]
	s_waitcnt lgkmcnt(0)
	v_add_f32_e32 v50, v50, v51
	global_atomic_add_f32 v[52:53], v50, off
.LBB0_2361:
	s_or_b64 exec, exec, s[22:23]
	v_add_u32_e32 v50, 0x90, v148
	s_waitcnt lgkmcnt(0)
	v_ashrrev_i32_e32 v51, 31, v50
	v_lshlrev_b64 v[52:53], 10, v[50:51]
	v_lshl_add_u64 v[60:61], v[52:53], 0, v[146:147]
	v_lshl_add_u64 v[62:63], v[60:61], 2, s[36:37]
	global_load_dwordx4 v[52:55], v[62:63], off
	global_load_dwordx4 v[56:59], v[62:63], off offset:16
	v_lshlrev_b64 v[60:61], 1, v[60:61]
	v_lshl_add_u64 v[64:65], s[80:81], 0, v[60:61]
	v_or_b32_e32 v60, 0x100, v60
	s_waitcnt vmcnt(1)
	v_pk_add_f32 v[54:55], v[48:49], v[54:55]
	v_pk_add_f32 v[52:53], v[46:47], v[52:53]
	s_waitcnt vmcnt(0)
	v_pk_add_f32 v[58:59], v[44:45], v[58:59]
	v_pk_add_f32 v[56:57], v[42:43], v[56:57]
	v_cvt_pk_bf16_f32 v42, v52, v53
	v_cvt_pk_bf16_f32 v43, v54, v55
	v_mul_f32_e32 v53, v53, v53
	v_cvt_pk_bf16_f32 v44, v56, v57
	v_cvt_pk_bf16_f32 v45, v58, v59
	global_store_dwordx4 v[64:65], v[42:45], off sc0 sc1
	global_load_dwordx4 v[42:45], v[62:63], off offset:512
	s_nop 0
	global_load_dwordx4 v[46:49], v[62:63], off offset:528
	v_mul_f32_e32 v55, v55, v55
	v_mul_f32_e32 v57, v57, v57
	v_mul_f32_e32 v59, v59, v59
	v_fmac_f32_e32 v53, v52, v52
	v_fmac_f32_e32 v55, v54, v54
	v_fmac_f32_e32 v57, v56, v56
	v_fmac_f32_e32 v59, v58, v58
	v_add_f32_e32 v52, v53, v55
	v_add_f32_e32 v53, v57, v59
	v_add_f32_e32 v52, v52, v53
	s_waitcnt vmcnt(1)
	v_pk_add_f32 v[40:41], v[40:41], v[44:45]
	v_pk_add_f32 v[38:39], v[38:39], v[42:43]
	s_waitcnt vmcnt(0)
	v_pk_add_f32 v[42:43], v[36:37], v[48:49]
	v_pk_add_f32 v[34:35], v[34:35], v[46:47]
	v_mul_f32_e32 v36, v39, v39
	v_mul_f32_e32 v37, v41, v41
	v_mul_f32_e32 v44, v35, v35
	v_mul_f32_e32 v45, v43, v43
	v_fmac_f32_e32 v36, v38, v38
	v_fmac_f32_e32 v37, v40, v40
	v_fmac_f32_e32 v44, v34, v34
	v_fmac_f32_e32 v45, v42, v42
	v_add_f32_e32 v36, v36, v37
	v_add_f32_e32 v37, v44, v45
	v_add_f32_e32 v36, v36, v37
	v_add_f32_e32 v44, v52, v36
	ds_bpermute_b32 v45, v122, v44
	v_cvt_pk_bf16_f32 v36, v38, v39
	v_cvt_pk_bf16_f32 v37, v40, v41
	v_cvt_pk_bf16_f32 v38, v34, v35
	v_lshl_add_u64 v[40:41], s[80:81], 0, v[60:61]
	s_waitcnt lgkmcnt(0)
	v_add_f32_e32 v34, v44, v45
	ds_bpermute_b32 v35, v116, v34
	v_cvt_pk_bf16_f32 v39, v42, v43
	global_store_dwordx4 v[40:41], v[36:39], off sc0 sc1
	s_and_saveexec_b64 s[22:23], s[4:5]
	s_cbranch_execz .LBB0_2363
	v_lshl_add_u64 v[36:37], v[50:51], 2, s[10:11]
	s_waitcnt lgkmcnt(0)
	v_add_f32_e32 v34, v34, v35
	global_atomic_add_f32 v[36:37], v34, off
; __device__ __forceinline__ unsigned cvt_pk_bf16(float lo, float hi) { unsigned r; asm volatile("v_cvt_pk_bf16_f32 %0, %1, %2" : "=v"(r) : "v"(lo), "v"(hi)); return r; }
;     __device__ __forceinline__ void operator()(const f32x4 (&acc)[2][2][4][2], const Unit& u, int wr, int wc, int fr, int fq) const {
;     ...
;                 const int row = row0 + ai * HALF + m * 16; const size_t off = (size_t)row * 1024 + col0; float s = 0.f;
; #pragma unroll
;                 for (int bj = 0; bj < 2; ++bj) { const size_t o2 = off + bj * HALF;
;                     f32x4 b0, b1;
;                     if (BASE_F32) { b0 = *(const f32x4*)(basef + o2); b1 = *(const f32x4*)(basef + o2 + 4); }
;                     else { const u32x4 p = *(const u32x4*)(xb + o2);
;                         b0 = (f32x4){__builtin_bit_cast(float, p.x << 16), __builtin_bit_cast(float, p.x & 0xffff0000u), __builtin_bit_cast(float, p.y << 16), __builtin_bit_cast(float, p.y & 0xffff0000u)};
;                         b1 = (f32x4){__builtin_bit_cast(float, p.z << 16), __builtin_bit_cast(float, p.z & 0xffff0000u), __builtin_bit_cast(float, p.w << 16), __builtin_bit_cast(float, p.w & 0xffff0000u)}; }
;                     const f32x4 o0 = b0 + acc[ai][bj][m][0], o1 = b1 + acc[ai][bj][m][1];
;                     s += ((o0[0] * o0[0] + o0[1] * o0[1]) + (o0[2] * o0[2] + o0[3] * o0[3])) + ((o1[0] * o1[0] + o1[1] * o1[1]) + (o1[2] * o1[2] + o1[3] * o1[3]));
;                     u32x4 w; w.x = cvt_pk_bf16(o0[0], o0[1]); w.y = cvt_pk_bf16(o0[2], o0[3]); w.z = cvt_pk_bf16(o1[0], o1[1]); w.w = cvt_pk_bf16(o1[2], o1[3]);
;                     *(u32x4*)(xb + o2) = w; }
;                 s += __shfl_xor(s, 16); s += __shfl_xor(s, 32);
;                 if (fq == 0) atomicAdd(ssq + row, s);
.LBB0_2363:
	s_or_b64 exec, exec, s[22:23]
	v_add_u32_e32 v34, 0xa0, v148
	s_waitcnt lgkmcnt(0)
	v_ashrrev_i32_e32 v35, 31, v34
	v_lshlrev_b64 v[36:37], 10, v[34:35]
	v_lshl_add_u64 v[44:45], v[36:37], 0, v[146:147]
	v_lshl_add_u64 v[46:47], v[44:45], 2, s[36:37]
	global_load_dwordx4 v[36:39], v[46:47], off
	global_load_dwordx4 v[40:43], v[46:47], off offset:16
	v_lshlrev_b64 v[44:45], 1, v[44:45]
	v_lshl_add_u64 v[48:49], s[80:81], 0, v[44:45]
	v_or_b32_e32 v44, 0x100, v44
	s_waitcnt vmcnt(1)
	v_pk_add_f32 v[38:39], v[32:33], v[38:39]
	v_pk_add_f32 v[36:37], v[30:31], v[36:37]
	s_waitcnt vmcnt(0)
	v_pk_add_f32 v[42:43], v[28:29], v[42:43]
	v_pk_add_f32 v[40:41], v[26:27], v[40:41]
	v_cvt_pk_bf16_f32 v26, v36, v37
	v_cvt_pk_bf16_f32 v27, v38, v39
	v_mul_f32_e32 v37, v37, v37
	v_cvt_pk_bf16_f32 v28, v40, v41
	v_cvt_pk_bf16_f32 v29, v42, v43
	global_store_dwordx4 v[48:49], v[26:29], off sc0 sc1
	global_load_dwordx4 v[26:29], v[46:47], off offset:512
	s_nop 0
	global_load_dwordx4 v[30:33], v[46:47], off offset:528
	v_mul_f32_e32 v39, v39, v39
	v_mul_f32_e32 v41, v41, v41
	v_mul_f32_e32 v43, v43, v43
	v_fmac_f32_e32 v37, v36, v36
	v_fmac_f32_e32 v39, v38, v38
	v_fmac_f32_e32 v41, v40, v40
	v_fmac_f32_e32 v43, v42, v42
	v_add_f32_e32 v36, v37, v39
	v_add_f32_e32 v37, v41, v43
	v_add_f32_e32 v36, v36, v37
	s_waitcnt vmcnt(1)
	v_pk_add_f32 v[24:25], v[24:25], v[28:29]
	v_pk_add_f32 v[22:23], v[22:23], v[26:27]
	s_waitcnt vmcnt(0)
	v_pk_add_f32 v[26:27], v[20:21], v[32:33]
	v_pk_add_f32 v[18:19], v[18:19], v[30:31]
	v_mul_f32_e32 v20, v23, v23
	v_mul_f32_e32 v21, v25, v25
	v_mul_f32_e32 v28, v19, v19
	v_mul_f32_e32 v29, v27, v27
	v_fmac_f32_e32 v20, v22, v22
	v_fmac_f32_e32 v21, v24, v24
	v_fmac_f32_e32 v28, v18, v18
	v_fmac_f32_e32 v29, v26, v26
	v_add_f32_e32 v20, v20, v21
	v_add_f32_e32 v21, v28, v29
	v_add_f32_e32 v20, v20, v21
	v_add_f32_e32 v28, v36, v20
	ds_bpermute_b32 v29, v122, v28
	v_cvt_pk_bf16_f32 v20, v22, v23
	v_cvt_pk_bf16_f32 v21, v24, v25
	v_cvt_pk_bf16_f32 v22, v18, v19
	v_lshl_add_u64 v[24:25], s[80:81], 0, v[44:45]
	s_waitcnt lgkmcnt(0)
	v_add_f32_e32 v18, v28, v29
	ds_bpermute_b32 v19, v116, v18
	v_cvt_pk_bf16_f32 v23, v26, v27
	global_store_dwordx4 v[24:25], v[20:23], off sc0 sc1
	s_and_saveexec_b64 s[22:23], s[4:5]
	s_cbranch_execz .LBB0_2365
	v_lshl_add_u64 v[20:21], v[34:35], 2, s[10:11]
	s_waitcnt lgkmcnt(0)
	v_add_f32_e32 v18, v18, v19
	global_atomic_add_f32 v[20:21], v18, off
.LBB0_2365:
	s_or_b64 exec, exec, s[22:23]
	v_add_u32_e32 v18, 0xb0, v148
	s_waitcnt lgkmcnt(0)
	v_ashrrev_i32_e32 v19, 31, v18
	v_lshlrev_b64 v[20:21], 10, v[18:19]
	v_lshl_add_u64 v[28:29], v[20:21], 0, v[146:147]
	v_lshl_add_u64 v[30:31], v[28:29], 2, s[36:37]
	global_load_dwordx4 v[20:23], v[30:31], off
	global_load_dwordx4 v[24:27], v[30:31], off offset:16
	v_lshlrev_b64 v[28:29], 1, v[28:29]
	v_lshl_add_u64 v[32:33], s[80:81], 0, v[28:29]
	v_or_b32_e32 v28, 0x100, v28
	s_waitcnt vmcnt(1)
	v_pk_add_f32 v[22:23], v[16:17], v[22:23]
	v_pk_add_f32 v[20:21], v[14:15], v[20:21]
	s_waitcnt vmcnt(0)
	v_pk_add_f32 v[26:27], v[12:13], v[26:27]
	v_pk_add_f32 v[24:25], v[10:11], v[24:25]
	v_cvt_pk_bf16_f32 v10, v20, v21
	v_cvt_pk_bf16_f32 v11, v22, v23
	v_mul_f32_e32 v21, v21, v21
	v_cvt_pk_bf16_f32 v12, v24, v25
	v_cvt_pk_bf16_f32 v13, v26, v27
	global_store_dwordx4 v[32:33], v[10:13], off sc0 sc1
	global_load_dwordx4 v[10:13], v[30:31], off offset:512
	s_nop 0
	global_load_dwordx4 v[14:17], v[30:31], off offset:528
	v_mul_f32_e32 v23, v23, v23
	v_mul_f32_e32 v25, v25, v25
	v_mul_f32_e32 v27, v27, v27
	v_fmac_f32_e32 v21, v20, v20
	v_fmac_f32_e32 v23, v22, v22
	v_fmac_f32_e32 v25, v24, v24
	v_fmac_f32_e32 v27, v26, v26
	v_add_f32_e32 v20, v21, v23
	v_add_f32_e32 v21, v25, v27
	v_add_f32_e32 v20, v20, v21
	s_waitcnt vmcnt(1)
	v_pk_add_f32 v[8:9], v[8:9], v[12:13]
	v_pk_add_f32 v[6:7], v[6:7], v[10:11]
	s_waitcnt vmcnt(0)
	v_pk_add_f32 v[10:11], v[4:5], v[16:17]
	v_pk_add_f32 v[2:3], v[2:3], v[14:15]
	v_mul_f32_e32 v4, v7, v7
	v_mul_f32_e32 v5, v9, v9
	v_mul_f32_e32 v12, v3, v3
	v_mul_f32_e32 v13, v11, v11
	v_fmac_f32_e32 v4, v6, v6
	v_fmac_f32_e32 v5, v8, v8
	v_fmac_f32_e32 v12, v2, v2
	v_fmac_f32_e32 v13, v10, v10
	v_add_f32_e32 v4, v4, v5
	v_add_f32_e32 v5, v12, v13
	v_add_f32_e32 v4, v4, v5
	v_add_f32_e32 v12, v20, v4
	ds_bpermute_b32 v13, v122, v12
	v_cvt_pk_bf16_f32 v4, v6, v7
	v_cvt_pk_bf16_f32 v5, v8, v9
	v_cvt_pk_bf16_f32 v6, v2, v3
	v_lshl_add_u64 v[8:9], s[80:81], 0, v[28:29]
	s_waitcnt lgkmcnt(0)
	v_add_f32_e32 v2, v12, v13
	ds_bpermute_b32 v3, v116, v2
	v_cvt_pk_bf16_f32 v7, v10, v11
	global_store_dwordx4 v[8:9], v[4:7], off sc0 sc1
	s_and_saveexec_b64 s[22:23], s[4:5]
	s_cbranch_execz .LBB0_2367
	v_lshl_add_u64 v[4:5], v[18:19], 2, s[10:11]
	s_waitcnt lgkmcnt(0)
	v_add_f32_e32 v2, v2, v3
	global_atomic_add_f32 v[4:5], v2, off

; __device__ __forceinline__ unsigned cvt_pk_bf16(float lo, float hi) { unsigned r; asm volatile("v_cvt_pk_bf16_f32 %0, %1, %2" : "=v"(r) : "v"(lo), "v"(hi)); return r; }
;     __device__ __forceinline__ void operator()(const f32x4 (&acc)[2][2][4][2], const Unit& u, int wr, int wc, int fr, int fq) const {
;         const int row0 = u.pm * BM + wr * 64 + fr, col0 = u.pn * BM + wc * 32 + 8 * fq;
; #pragma unroll
;         for (int ai = 0; ai < 2; ++ai)
; #pragma unroll
;             for (int m = 0; m < 4; ++m) {
;                 const int row = row0 + ai * HALF + m * 16; const size_t off = (size_t)row * 1024 + col0; float s = 0.f;
; #pragma unroll
;                 for (int bj = 0; bj < 2; ++bj) { const size_t o2 = off + bj * HALF;
;                     f32x4 b0, b1;
;                     if (BASE_F32) { b0 = *(const f32x4*)(basef + o2); b1 = *(const f32x4*)(basef + o2 + 4); }
;                     else { const u32x4 p = *(const u32x4*)(xb + o2);
;                         b0 = (f32x4){__builtin_bit_cast(float, p.x << 16), __builtin_bit_cast(float, p.x & 0xffff0000u), __builtin_bit_cast(float, p.y << 16), __builtin_bit_cast(float, p.y & 0xffff0000u)};
;                         b1 = (f32x4){__builtin_bit_cast(float, p.z << 16), __builtin_bit_cast(float, p.z & 0xffff0000u), __builtin_bit_cast(float, p.w << 16), __builtin_bit_cast(float, p.w & 0xffff0000u)}; }
;                     const f32x4 o0 = b0 + acc[ai][bj][m][0], o1 = b1 + acc[ai][bj][m][1];
;                     s += ((o0[0] * o0[0] + o0[1] * o0[1]) + (o0[2] * o0[2] + o0[3] * o0[3])) + ((o1[0] * o1[0] + o1[1] * o1[1]) + (o1[2] * o1[2] + o1[3] * o1[3]));
;                     u32x4 w; w.x = cvt_pk_bf16(o0[0], o0[1]); w.y = cvt_pk_bf16(o0[2], o0[3]); w.z = cvt_pk_bf16(o1[0], o1[1]); w.w = cvt_pk_bf16(o1[2], o1[3]);
;                     *(u32x4*)(xb + o2) = w; }
;                 s += __shfl_xor(s, 16); s += __shfl_xor(s, 32);
;                 if (fq == 0) atomicAdd(ssq + row, s);
.LBB0_2525:
	v_lshl_add_u32 v148, s38, 8, v1
	v_ashrrev_i32_e32 v149, 31, v148
	v_lshl_or_b32 v146, s40, 8, v151
	v_lshlrev_b64 v[156:157], 11, v[148:149]
	v_ashrrev_i32_e32 v147, 31, v146
	v_lshl_add_u64 v[156:157], s[80:81], 0, v[156:157]
	v_lshl_add_u64 v[160:161], v[146:147], 1, v[156:157]
	global_load_dwordx4 v[156:159], v[160:161], off
	v_xor_b32_e32 v168, 32, v155
	s_waitcnt vmcnt(0)
	v_lshlrev_b32_e32 v162, 16, v156
	v_and_b32_e32 v163, 0xffff0000, v156
	v_lshlrev_b32_e32 v156, 16, v157
	v_and_b32_e32 v157, 0xffff0000, v157
	v_lshlrev_b32_e32 v164, 16, v158
	v_and_b32_e32 v165, 0xffff0000, v158
	v_lshlrev_b32_e32 v158, 16, v159
	v_and_b32_e32 v159, 0xffff0000, v159
	v_pk_add_f32 v[128:129], v[128:129], v[156:157]
	v_pk_add_f32 v[162:163], v[126:127], v[162:163]
	v_pk_add_f32 v[166:167], v[124:125], v[158:159]
	v_pk_add_f32 v[164:165], v[122:123], v[164:165]
	v_cvt_pk_bf16_f32 v124, v162, v163
	v_cvt_pk_bf16_f32 v125, v128, v129
	v_mul_f32_e32 v163, v163, v163
	v_cvt_pk_bf16_f32 v126, v164, v165
	v_cvt_pk_bf16_f32 v127, v166, v167
	global_load_dwordx4 v[156:159], v[160:161], off offset:256
	v_mul_f32_e32 v129, v129, v129
	v_mul_f32_e32 v165, v165, v165
	v_mul_f32_e32 v167, v167, v167
	v_fmac_f32_e32 v163, v162, v162
	v_fmac_f32_e32 v129, v128, v128
	v_fmac_f32_e32 v165, v164, v164
	v_fmac_f32_e32 v167, v166, v166
	v_add_f32_e32 v128, v163, v129
	v_add_f32_e32 v129, v165, v167
	v_add_f32_e32 v164, v128, v129
	v_and_b32_e32 v123, 64, v155
	v_xor_b32_e32 v122, 16, v155
	v_add_u32_e32 v123, 64, v123
	v_cmp_lt_i32_e32 vcc, v122, v123
	global_store_dwordx4 v[160:161], v[124:127], off sc0 sc1
	s_waitcnt vmcnt(1)
	v_lshlrev_b32_e32 v128, 16, v156
	v_and_b32_e32 v129, 0xffff0000, v156
	v_lshlrev_b32_e32 v156, 16, v157
	v_and_b32_e32 v157, 0xffff0000, v157
	v_lshlrev_b32_e32 v162, 16, v158
	v_and_b32_e32 v163, 0xffff0000, v158
	v_lshlrev_b32_e32 v158, 16, v159
	v_and_b32_e32 v159, 0xffff0000, v159
	v_pk_add_f32 v[120:121], v[120:121], v[156:157]
	v_pk_add_f32 v[118:119], v[118:119], v[128:129]
	v_pk_add_f32 v[128:129], v[116:117], v[158:159]
	v_pk_add_f32 v[156:157], v[114:115], v[162:163]
	v_mul_f32_e32 v114, v119, v119
	v_mul_f32_e32 v115, v121, v121
	v_mul_f32_e32 v116, v157, v157
	v_mul_f32_e32 v117, v129, v129
	v_fmac_f32_e32 v114, v118, v118
	v_fmac_f32_e32 v115, v120, v120
	v_fmac_f32_e32 v116, v156, v156
	v_fmac_f32_e32 v117, v128, v128
	v_add_f32_e32 v114, v114, v115
	v_add_f32_e32 v115, v116, v117
	v_cndmask_b32_e32 v122, v155, v122, vcc
	v_add_f32_e32 v114, v114, v115
	v_lshlrev_b32_e32 v122, 2, v122
	v_add_f32_e32 v114, v164, v114
	ds_bpermute_b32 v115, v122, v114
	v_cmp_lt_i32_e32 vcc, v168, v123
	v_cvt_pk_bf16_f32 v118, v118, v119
	v_cvt_pk_bf16_f32 v119, v120, v121
	v_cvt_pk_bf16_f32 v120, v156, v157
	s_waitcnt lgkmcnt(0)
	v_add_f32_e32 v114, v114, v115
	v_cvt_pk_bf16_f32 v121, v128, v129
	v_cndmask_b32_e32 v116, v155, v168, vcc
	v_lshlrev_b32_e32 v116, 2, v116
	ds_bpermute_b32 v115, v116, v114
	global_store_dwordx4 v[160:161], v[118:121], off offset:256 sc0 sc1
	s_and_saveexec_b64 s[22:23], s[4:5]
	s_cbranch_execz .LBB0_2527
	s_waitcnt lgkmcnt(0)
	v_add_f32_e32 v117, v114, v115
	v_lshl_add_u64 v[114:115], v[148:149], 2, s[10:11]
	global_atomic_add_f32 v[114:115], v117, off
.LBB0_2527:
	s_or_b64 exec, exec, s[22:23]
	v_or_b32_e32 v114, 16, v148
	s_waitcnt lgkmcnt(0)
	v_ashrrev_i32_e32 v115, 31, v114
	v_lshlrev_b64 v[118:119], 11, v[114:115]
	v_lshl_add_u64 v[118:119], s[80:81], 0, v[118:119]
	v_lshl_add_u64 v[124:125], v[146:147], 1, v[118:119]
	global_load_dwordx4 v[118:121], v[124:125], off
	s_waitcnt vmcnt(0)
	v_lshlrev_b32_e32 v126, 16, v118
	v_and_b32_e32 v127, 0xffff0000, v118
	v_lshlrev_b32_e32 v118, 16, v119
	v_and_b32_e32 v119, 0xffff0000, v119
	v_lshlrev_b32_e32 v128, 16, v120
	v_and_b32_e32 v129, 0xffff0000, v120
	v_lshlrev_b32_e32 v120, 16, v121
	v_and_b32_e32 v121, 0xffff0000, v121
	v_pk_add_f32 v[118:119], v[112:113], v[118:119]
	v_pk_add_f32 v[126:127], v[110:111], v[126:127]
	v_pk_add_f32 v[120:121], v[108:109], v[120:121]
	v_pk_add_f32 v[128:129], v[106:107], v[128:129]
	v_cvt_pk_bf16_f32 v106, v126, v127
	v_cvt_pk_bf16_f32 v107, v118, v119
	v_mul_f32_e32 v117, v127, v127
	v_cvt_pk_bf16_f32 v108, v128, v129
	v_cvt_pk_bf16_f32 v109, v120, v121
	global_load_dwordx4 v[110:113], v[124:125], off offset:256
	v_mul_f32_e32 v119, v119, v119
	v_mul_f32_e32 v123, v129, v129
	v_mul_f32_e32 v121, v121, v121
	v_fmac_f32_e32 v117, v126, v126
	v_fmac_f32_e32 v119, v118, v118
	v_fmac_f32_e32 v123, v128, v128
	v_fmac_f32_e32 v121, v120, v120
	v_add_f32_e32 v117, v117, v119
	v_add_f32_e32 v118, v123, v121
	v_add_f32_e32 v117, v117, v118
	global_store_dwordx4 v[124:125], v[106:109], off sc0 sc1
	s_waitcnt vmcnt(1)
	v_lshlrev_b32_e32 v118, 16, v110
	v_and_b32_e32 v119, 0xffff0000, v110
	v_lshlrev_b32_e32 v110, 16, v111
	v_and_b32_e32 v111, 0xffff0000, v111
	v_lshlrev_b32_e32 v120, 16, v112
	v_and_b32_e32 v121, 0xffff0000, v112
	v_lshlrev_b32_e32 v112, 16, v113
	v_and_b32_e32 v113, 0xffff0000, v113
	v_pk_add_f32 v[104:105], v[104:105], v[110:111]
	v_pk_add_f32 v[102:103], v[102:103], v[118:119]
	v_pk_add_f32 v[110:111], v[100:101], v[112:113]
	v_pk_add_f32 v[112:113], v[98:99], v[120:121]
	v_mul_f32_e32 v98, v103, v103
	v_mul_f32_e32 v99, v105, v105
	v_mul_f32_e32 v100, v113, v113
	v_mul_f32_e32 v101, v111, v111
	v_fmac_f32_e32 v98, v102, v102
	v_fmac_f32_e32 v99, v104, v104
	v_fmac_f32_e32 v100, v112, v112
	v_fmac_f32_e32 v101, v110, v110
	v_add_f32_e32 v98, v98, v99
	v_add_f32_e32 v99, v100, v101
	v_add_f32_e32 v98, v98, v99
	v_add_f32_e32 v98, v117, v98
	ds_bpermute_b32 v99, v122, v98
	v_cvt_pk_bf16_f32 v100, v102, v103
	v_cvt_pk_bf16_f32 v101, v104, v105
	v_cvt_pk_bf16_f32 v102, v112, v113
	v_cvt_pk_bf16_f32 v103, v110, v111
	s_waitcnt lgkmcnt(0)
	v_add_f32_e32 v98, v98, v99
	ds_bpermute_b32 v99, v116, v98
	global_store_dwordx4 v[124:125], v[100:103], off offset:256 sc0 sc1
	s_and_saveexec_b64 s[22:23], s[4:5]
	s_cbranch_execz .LBB0_2529
	s_waitcnt lgkmcnt(0)
	v_add_f32_e32 v100, v98, v99
	v_lshl_add_u64 v[98:99], v[114:115], 2, s[10:11]
	global_atomic_add_f32 v[98:99], v100, off
; __device__ __forceinline__ unsigned cvt_pk_bf16(float lo, float hi) { unsigned r; asm volatile("v_cvt_pk_bf16_f32 %0, %1, %2" : "=v"(r) : "v"(lo), "v"(hi)); return r; }
;     __device__ __forceinline__ void operator()(const f32x4 (&acc)[2][2][4][2], const Unit& u, int wr, int wc, int fr, int fq) const {
;         const int row0 = u.pm * BM + wr * 64 + fr, col0 = u.pn * BM + wc * 32 + 8 * fq;
; #pragma unroll
;         for (int ai = 0; ai < 2; ++ai)
; #pragma unroll
;             for (int m = 0; m < 4; ++m) {
;                 const int row = row0 + ai * HALF + m * 16; const size_t off = (size_t)row * 1024 + col0; float s = 0.f;
; #pragma unroll
;                 for (int bj = 0; bj < 2; ++bj) { const size_t o2 = off + bj * HALF;
;                     f32x4 b0, b1;
;                     if (BASE_F32) { b0 = *(const f32x4*)(basef + o2); b1 = *(const f32x4*)(basef + o2 + 4); }
;                     else { const u32x4 p = *(const u32x4*)(xb + o2);
;                         b0 = (f32x4){__builtin_bit_cast(float, p.x << 16), __builtin_bit_cast(float, p.x & 0xffff0000u), __builtin_bit_cast(float, p.y << 16), __builtin_bit_cast(float, p.y & 0xffff0000u)};
;                         b1 = (f32x4){__builtin_bit_cast(float, p.z << 16), __builtin_bit_cast(float, p.z & 0xffff0000u), __builtin_bit_cast(float, p.w << 16), __builtin_bit_cast(float, p.w & 0xffff0000u)}; }
;                     const f32x4 o0 = b0 + acc[ai][bj][m][0], o1 = b1 + acc[ai][bj][m][1];
;                     s += ((o0[0] * o0[0] + o0[1] * o0[1]) + (o0[2] * o0[2] + o0[3] * o0[3])) + ((o1[0] * o1[0] + o1[1] * o1[1]) + (o1[2] * o1[2] + o1[3] * o1[3]));
;                     u32x4 w; w.x = cvt_pk_bf16(o0[0], o0[1]); w.y = cvt_pk_bf16(o0[2], o0[3]); w.z = cvt_pk_bf16(o1[0], o1[1]); w.w = cvt_pk_bf16(o1[2], o1[3]);
;                     *(u32x4*)(xb + o2) = w; }
;                 s += __shfl_xor(s, 16); s += __shfl_xor(s, 32);
;                 if (fq == 0) atomicAdd(ssq + row, s);
.LBB0_2529:
	s_or_b64 exec, exec, s[22:23]
	v_or_b32_e32 v98, 32, v148
	s_waitcnt lgkmcnt(0)
	v_ashrrev_i32_e32 v99, 31, v98
	v_lshlrev_b64 v[100:101], 11, v[98:99]
	v_lshl_add_u64 v[100:101], s[80:81], 0, v[100:101]
	v_lshl_add_u64 v[104:105], v[146:147], 1, v[100:101]
	global_load_dwordx4 v[100:103], v[104:105], off
	s_waitcnt vmcnt(0)
	v_lshlrev_b32_e32 v106, 16, v100
	v_and_b32_e32 v107, 0xffff0000, v100
	v_lshlrev_b32_e32 v100, 16, v101
	v_and_b32_e32 v101, 0xffff0000, v101
	v_lshlrev_b32_e32 v108, 16, v102
	v_and_b32_e32 v109, 0xffff0000, v102
	v_lshlrev_b32_e32 v102, 16, v103
	v_and_b32_e32 v103, 0xffff0000, v103
	v_pk_add_f32 v[100:101], v[96:97], v[100:101]
	v_pk_add_f32 v[106:107], v[94:95], v[106:107]
	v_pk_add_f32 v[102:103], v[92:93], v[102:103]
	v_pk_add_f32 v[108:109], v[90:91], v[108:109]
	v_cvt_pk_bf16_f32 v90, v106, v107
	v_cvt_pk_bf16_f32 v91, v100, v101
	v_mul_f32_e32 v107, v107, v107
	v_cvt_pk_bf16_f32 v92, v108, v109
	v_cvt_pk_bf16_f32 v93, v102, v103
	global_load_dwordx4 v[94:97], v[104:105], off offset:256
	v_mul_f32_e32 v101, v101, v101
	v_mul_f32_e32 v109, v109, v109
	v_mul_f32_e32 v103, v103, v103
	v_fmac_f32_e32 v107, v106, v106
	v_fmac_f32_e32 v101, v100, v100
	v_fmac_f32_e32 v109, v108, v108
	v_fmac_f32_e32 v103, v102, v102
	v_add_f32_e32 v100, v107, v101
	v_add_f32_e32 v101, v109, v103
	v_add_f32_e32 v106, v100, v101
	global_store_dwordx4 v[104:105], v[90:93], off sc0 sc1
	s_waitcnt vmcnt(1)
	v_lshlrev_b32_e32 v100, 16, v94
	v_and_b32_e32 v101, 0xffff0000, v94
	v_lshlrev_b32_e32 v94, 16, v95
	v_and_b32_e32 v95, 0xffff0000, v95
	v_lshlrev_b32_e32 v102, 16, v96
	v_and_b32_e32 v103, 0xffff0000, v96
	v_lshlrev_b32_e32 v96, 16, v97
	v_and_b32_e32 v97, 0xffff0000, v97
	v_pk_add_f32 v[88:89], v[88:89], v[94:95]
	v_pk_add_f32 v[86:87], v[86:87], v[100:101]
	v_pk_add_f32 v[94:95], v[84:85], v[96:97]
	v_pk_add_f32 v[96:97], v[82:83], v[102:103]
	v_mul_f32_e32 v82, v87, v87
	v_mul_f32_e32 v83, v89, v89
	v_mul_f32_e32 v84, v97, v97
	v_mul_f32_e32 v85, v95, v95
	v_fmac_f32_e32 v82, v86, v86
	v_fmac_f32_e32 v83, v88, v88
	v_fmac_f32_e32 v84, v96, v96
	v_fmac_f32_e32 v85, v94, v94
	v_add_f32_e32 v82, v82, v83
	v_add_f32_e32 v83, v84, v85
	v_add_f32_e32 v82, v82, v83
	v_add_f32_e32 v82, v106, v82
	ds_bpermute_b32 v83, v122, v82
	v_cvt_pk_bf16_f32 v84, v86, v87
	v_cvt_pk_bf16_f32 v85, v88, v89
	v_cvt_pk_bf16_f32 v86, v96, v97
	v_cvt_pk_bf16_f32 v87, v94, v95
	s_waitcnt lgkmcnt(0)
	v_add_f32_e32 v82, v82, v83
	ds_bpermute_b32 v83, v116, v82
	global_store_dwordx4 v[104:105], v[84:87], off offset:256 sc0 sc1
	s_and_saveexec_b64 s[22:23], s[4:5]
	s_cbranch_execz .LBB0_2531
	s_waitcnt lgkmcnt(0)
	v_add_f32_e32 v84, v82, v83
	v_lshl_add_u64 v[82:83], v[98:99], 2, s[10:11]
	global_atomic_add_f32 v[82:83], v84, off
.LBB0_2531:
	s_or_b64 exec, exec, s[22:23]
	v_or_b32_e32 v82, 48, v148
	s_waitcnt lgkmcnt(0)
	v_ashrrev_i32_e32 v83, 31, v82
	v_lshlrev_b64 v[84:85], 11, v[82:83]
	v_lshl_add_u64 v[84:85], s[80:81], 0, v[84:85]
	v_lshl_add_u64 v[88:89], v[146:147], 1, v[84:85]
	global_load_dwordx4 v[84:87], v[88:89], off
	s_waitcnt vmcnt(0)
	v_lshlrev_b32_e32 v90, 16, v84
	v_and_b32_e32 v91, 0xffff0000, v84
	v_lshlrev_b32_e32 v84, 16, v85
	v_and_b32_e32 v85, 0xffff0000, v85
	v_lshlrev_b32_e32 v92, 16, v86
	v_and_b32_e32 v93, 0xffff0000, v86
	v_lshlrev_b32_e32 v86, 16, v87
	v_and_b32_e32 v87, 0xffff0000, v87
	v_pk_add_f32 v[84:85], v[80:81], v[84:85]
	v_pk_add_f32 v[90:91], v[78:79], v[90:91]
	v_pk_add_f32 v[86:87], v[76:77], v[86:87]
	v_pk_add_f32 v[92:93], v[74:75], v[92:93]
	v_cvt_pk_bf16_f32 v74, v90, v91
	v_cvt_pk_bf16_f32 v75, v84, v85
	v_mul_f32_e32 v91, v91, v91
	v_cvt_pk_bf16_f32 v76, v92, v93
	v_cvt_pk_bf16_f32 v77, v86, v87
	global_load_dwordx4 v[78:81], v[88:89], off offset:256
	v_mul_f32_e32 v85, v85, v85
	v_mul_f32_e32 v93, v93, v93
	v_mul_f32_e32 v87, v87, v87
	v_fmac_f32_e32 v91, v90, v90
	v_fmac_f32_e32 v85, v84, v84
	v_fmac_f32_e32 v93, v92, v92
	v_fmac_f32_e32 v87, v86, v86
	v_add_f32_e32 v84, v91, v85
	v_add_f32_e32 v85, v93, v87
	v_add_f32_e32 v90, v84, v85
	global_store_dwordx4 v[88:89], v[74:77], off sc0 sc1
	s_waitcnt vmcnt(1)
	v_lshlrev_b32_e32 v84, 16, v78
	v_and_b32_e32 v85, 0xffff0000, v78
	v_lshlrev_b32_e32 v78, 16, v79
	v_and_b32_e32 v79, 0xffff0000, v79
	v_lshlrev_b32_e32 v86, 16, v80
	v_and_b32_e32 v87, 0xffff0000, v80
	v_lshlrev_b32_e32 v80, 16, v81
	v_and_b32_e32 v81, 0xffff0000, v81
	v_pk_add_f32 v[72:73], v[72:73], v[78:79]
	v_pk_add_f32 v[70:71], v[70:71], v[84:85]
	v_pk_add_f32 v[78:79], v[68:69], v[80:81]
	v_pk_add_f32 v[80:81], v[66:67], v[86:87]
	v_mul_f32_e32 v66, v71, v71
	v_mul_f32_e32 v67, v73, v73
	v_mul_f32_e32 v68, v81, v81
	v_mul_f32_e32 v69, v79, v79
	v_fmac_f32_e32 v66, v70, v70
	v_fmac_f32_e32 v67, v72, v72
	v_fmac_f32_e32 v68, v80, v80
	v_fmac_f32_e32 v69, v78, v78
	v_add_f32_e32 v66, v66, v67
	v_add_f32_e32 v67, v68, v69
	v_add_f32_e32 v66, v66, v67
	v_add_f32_e32 v66, v90, v66
	ds_bpermute_b32 v67, v122, v66
	v_cvt_pk_bf16_f32 v68, v70, v71
	v_cvt_pk_bf16_f32 v69, v72, v73
	v_cvt_pk_bf16_f32 v70, v80, v81
	v_cvt_pk_bf16_f32 v71, v78, v79
	s_waitcnt lgkmcnt(0)
	v_add_f32_e32 v66, v66, v67
	ds_bpermute_b32 v67, v116, v66
	global_store_dwordx4 v[88:89], v[68:71], off offset:256 sc0 sc1
	s_and_saveexec_b64 s[22:23], s[4:5]
	s_cbranch_execz .LBB0_2533
	s_waitcnt lgkmcnt(0)
	v_add_f32_e32 v68, v66, v67
	v_lshl_add_u64 v[66:67], v[82:83], 2, s[10:11]
	global_atomic_add_f32 v[66:67], v68, off
; __device__ __forceinline__ unsigned cvt_pk_bf16(float lo, float hi) { unsigned r; asm volatile("v_cvt_pk_bf16_f32 %0, %1, %2" : "=v"(r) : "v"(lo), "v"(hi)); return r; }
;     __device__ __forceinline__ void operator()(const f32x4 (&acc)[2][2][4][2], const Unit& u, int wr, int wc, int fr, int fq) const {
;         const int row0 = u.pm * BM + wr * 64 + fr, col0 = u.pn * BM + wc * 32 + 8 * fq;
; #pragma unroll
;         for (int ai = 0; ai < 2; ++ai)
; #pragma unroll
;             for (int m = 0; m < 4; ++m) {
;                 const int row = row0 + ai * HALF + m * 16; const size_t off = (size_t)row * 1024 + col0; float s = 0.f;
; #pragma unroll
;                 for (int bj = 0; bj < 2; ++bj) { const size_t o2 = off + bj * HALF;
;                     f32x4 b0, b1;
;                     if (BASE_F32) { b0 = *(const f32x4*)(basef + o2); b1 = *(const f32x4*)(basef + o2 + 4); }
;                     else { const u32x4 p = *(const u32x4*)(xb + o2);
;                         b0 = (f32x4){__builtin_bit_cast(float, p.x << 16), __builtin_bit_cast(float, p.x & 0xffff0000u), __builtin_bit_cast(float, p.y << 16), __builtin_bit_cast(float, p.y & 0xffff0000u)};
;                         b1 = (f32x4){__builtin_bit_cast(float, p.z << 16), __builtin_bit_cast(float, p.z & 0xffff0000u), __builtin_bit_cast(float, p.w << 16), __builtin_bit_cast(float, p.w & 0xffff0000u)}; }
;                     const f32x4 o0 = b0 + acc[ai][bj][m][0], o1 = b1 + acc[ai][bj][m][1];
;                     s += ((o0[0] * o0[0] + o0[1] * o0[1]) + (o0[2] * o0[2] + o0[3] * o0[3])) + ((o1[0] * o1[0] + o1[1] * o1[1]) + (o1[2] * o1[2] + o1[3] * o1[3]));
;                     u32x4 w; w.x = cvt_pk_bf16(o0[0], o0[1]); w.y = cvt_pk_bf16(o0[2], o0[3]); w.z = cvt_pk_bf16(o1[0], o1[1]); w.w = cvt_pk_bf16(o1[2], o1[3]);
;                     *(u32x4*)(xb + o2) = w; }
;                 s += __shfl_xor(s, 16); s += __shfl_xor(s, 32);
;                 if (fq == 0) atomicAdd(ssq + row, s);
.LBB0_2533:
	s_or_b64 exec, exec, s[22:23]
	v_add_u32_e32 v66, 0x80, v148
	s_waitcnt lgkmcnt(0)
	v_ashrrev_i32_e32 v67, 31, v66
	v_lshlrev_b64 v[68:69], 11, v[66:67]
	v_lshl_add_u64 v[68:69], s[80:81], 0, v[68:69]
	v_lshl_add_u64 v[72:73], v[146:147], 1, v[68:69]
	global_load_dwordx4 v[68:71], v[72:73], off
	s_waitcnt vmcnt(0)
	v_lshlrev_b32_e32 v74, 16, v68
	v_and_b32_e32 v75, 0xffff0000, v68
	v_lshlrev_b32_e32 v68, 16, v69
	v_and_b32_e32 v69, 0xffff0000, v69
	v_lshlrev_b32_e32 v76, 16, v70
	v_and_b32_e32 v77, 0xffff0000, v70
	v_lshlrev_b32_e32 v70, 16, v71
	v_and_b32_e32 v71, 0xffff0000, v71
	v_pk_add_f32 v[68:69], v[64:65], v[68:69]
	v_pk_add_f32 v[74:75], v[62:63], v[74:75]
	v_pk_add_f32 v[70:71], v[60:61], v[70:71]
	v_pk_add_f32 v[76:77], v[58:59], v[76:77]
	v_cvt_pk_bf16_f32 v58, v74, v75
	v_cvt_pk_bf16_f32 v59, v68, v69
	v_mul_f32_e32 v75, v75, v75
	v_cvt_pk_bf16_f32 v60, v76, v77
	v_cvt_pk_bf16_f32 v61, v70, v71
	global_load_dwordx4 v[62:65], v[72:73], off offset:256
	v_mul_f32_e32 v69, v69, v69
	v_mul_f32_e32 v77, v77, v77
	v_mul_f32_e32 v71, v71, v71
	v_fmac_f32_e32 v75, v74, v74
	v_fmac_f32_e32 v69, v68, v68
	v_fmac_f32_e32 v77, v76, v76
	v_fmac_f32_e32 v71, v70, v70
	v_add_f32_e32 v68, v75, v69
	v_add_f32_e32 v69, v77, v71
	v_add_f32_e32 v74, v68, v69
	global_store_dwordx4 v[72:73], v[58:61], off sc0 sc1
	s_waitcnt vmcnt(1)
	v_lshlrev_b32_e32 v68, 16, v62
	v_and_b32_e32 v69, 0xffff0000, v62
	v_lshlrev_b32_e32 v62, 16, v63
	v_and_b32_e32 v63, 0xffff0000, v63
	v_lshlrev_b32_e32 v70, 16, v64
	v_and_b32_e32 v71, 0xffff0000, v64
	v_lshlrev_b32_e32 v64, 16, v65
	v_and_b32_e32 v65, 0xffff0000, v65
	v_pk_add_f32 v[56:57], v[56:57], v[62:63]
	v_pk_add_f32 v[54:55], v[54:55], v[68:69]
	v_pk_add_f32 v[62:63], v[52:53], v[64:65]
	v_pk_add_f32 v[64:65], v[50:51], v[70:71]
	v_mul_f32_e32 v50, v55, v55
	v_mul_f32_e32 v51, v57, v57
	v_mul_f32_e32 v52, v65, v65
	v_mul_f32_e32 v53, v63, v63
	v_fmac_f32_e32 v50, v54, v54
	v_fmac_f32_e32 v51, v56, v56
	v_fmac_f32_e32 v52, v64, v64
	v_fmac_f32_e32 v53, v62, v62
	v_add_f32_e32 v50, v50, v51
	v_add_f32_e32 v51, v52, v53
	v_add_f32_e32 v50, v50, v51
	v_add_f32_e32 v50, v74, v50
	ds_bpermute_b32 v51, v122, v50
	v_cvt_pk_bf16_f32 v52, v54, v55
	v_cvt_pk_bf16_f32 v53, v56, v57
	v_cvt_pk_bf16_f32 v54, v64, v65
	v_cvt_pk_bf16_f32 v55, v62, v63
	s_waitcnt lgkmcnt(0)
	v_add_f32_e32 v50, v50, v51
	ds_bpermute_b32 v51, v116, v50
	global_store_dwordx4 v[72:73], v[52:55], off offset:256 sc0 sc1
	s_and_saveexec_b64 s[22:23], s[4:5]
	s_cbranch_execz .LBB0_2535
	s_waitcnt lgkmcnt(0)
	v_add_f32_e32 v52, v50, v51
	v_lshl_add_u64 v[50:51], v[66:67], 2, s[10:11]
	global_atomic_add_f32 v[50:51], v52, off
.LBB0_2535:
	s_or_b64 exec, exec, s[22:23]
	v_add_u32_e32 v50, 0x90, v148
	s_waitcnt lgkmcnt(0)
	v_ashrrev_i32_e32 v51, 31, v50
	v_lshlrev_b64 v[52:53], 11, v[50:51]
	v_lshl_add_u64 v[52:53], s[80:81], 0, v[52:53]
	v_lshl_add_u64 v[56:57], v[146:147], 1, v[52:53]
	global_load_dwordx4 v[52:55], v[56:57], off
	s_waitcnt vmcnt(0)
	v_lshlrev_b32_e32 v58, 16, v52
	v_and_b32_e32 v59, 0xffff0000, v52
	v_lshlrev_b32_e32 v52, 16, v53
	v_and_b32_e32 v53, 0xffff0000, v53
	v_lshlrev_b32_e32 v60, 16, v54
	v_and_b32_e32 v61, 0xffff0000, v54
	v_lshlrev_b32_e32 v54, 16, v55
	v_and_b32_e32 v55, 0xffff0000, v55
	v_pk_add_f32 v[52:53], v[48:49], v[52:53]
	v_pk_add_f32 v[58:59], v[46:47], v[58:59]
	v_pk_add_f32 v[54:55], v[44:45], v[54:55]
	v_pk_add_f32 v[60:61], v[42:43], v[60:61]
	v_cvt_pk_bf16_f32 v42, v58, v59
	v_cvt_pk_bf16_f32 v43, v52, v53
	v_mul_f32_e32 v59, v59, v59
	v_cvt_pk_bf16_f32 v44, v60, v61
	v_cvt_pk_bf16_f32 v45, v54, v55
	global_load_dwordx4 v[46:49], v[56:57], off offset:256
	v_mul_f32_e32 v53, v53, v53
	v_mul_f32_e32 v61, v61, v61
	v_mul_f32_e32 v55, v55, v55
	v_fmac_f32_e32 v59, v58, v58
	v_fmac_f32_e32 v53, v52, v52
	v_fmac_f32_e32 v61, v60, v60
	v_fmac_f32_e32 v55, v54, v54
	v_add_f32_e32 v52, v59, v53
	v_add_f32_e32 v53, v61, v55
	v_add_f32_e32 v58, v52, v53
	global_store_dwordx4 v[56:57], v[42:45], off sc0 sc1
	s_waitcnt vmcnt(1)
	v_lshlrev_b32_e32 v52, 16, v46
	v_and_b32_e32 v53, 0xffff0000, v46
	v_lshlrev_b32_e32 v46, 16, v47
	v_and_b32_e32 v47, 0xffff0000, v47
	v_lshlrev_b32_e32 v54, 16, v48
	v_and_b32_e32 v55, 0xffff0000, v48
	v_lshlrev_b32_e32 v48, 16, v49
	v_and_b32_e32 v49, 0xffff0000, v49
	v_pk_add_f32 v[40:41], v[40:41], v[46:47]
	v_pk_add_f32 v[38:39], v[38:39], v[52:53]
	v_pk_add_f32 v[46:47], v[36:37], v[48:49]
	v_pk_add_f32 v[48:49], v[34:35], v[54:55]
	v_mul_f32_e32 v34, v39, v39
	v_mul_f32_e32 v35, v41, v41
	v_mul_f32_e32 v36, v49, v49
	v_mul_f32_e32 v37, v47, v47
	v_fmac_f32_e32 v34, v38, v38
	v_fmac_f32_e32 v35, v40, v40
	v_fmac_f32_e32 v36, v48, v48
	v_fmac_f32_e32 v37, v46, v46
	v_add_f32_e32 v34, v34, v35
	v_add_f32_e32 v35, v36, v37
	v_add_f32_e32 v34, v34, v35
	v_add_f32_e32 v34, v58, v34
	ds_bpermute_b32 v35, v122, v34
	v_cvt_pk_bf16_f32 v36, v38, v39
	v_cvt_pk_bf16_f32 v37, v40, v41
	v_cvt_pk_bf16_f32 v38, v48, v49
	v_cvt_pk_bf16_f32 v39, v46, v47
	s_waitcnt lgkmcnt(0)
	v_add_f32_e32 v34, v34, v35
	ds_bpermute_b32 v35, v116, v34
	global_store_dwordx4 v[56:57], v[36:39], off offset:256 sc0 sc1
	s_and_saveexec_b64 s[22:23], s[4:5]
	s_cbranch_execz .LBB0_2537
	s_waitcnt lgkmcnt(0)
	v_add_f32_e32 v36, v34, v35
	v_lshl_add_u64 v[34:35], v[50:51], 2, s[10:11]
	global_atomic_add_f32 v[34:35], v36, off
; __device__ __forceinline__ unsigned cvt_pk_bf16(float lo, float hi) { unsigned r; asm volatile("v_cvt_pk_bf16_f32 %0, %1, %2" : "=v"(r) : "v"(lo), "v"(hi)); return r; }
;     __device__ __forceinline__ void operator()(const f32x4 (&acc)[2][2][4][2], const Unit& u, int wr, int wc, int fr, int fq) const {
;         const int row0 = u.pm * BM + wr * 64 + fr, col0 = u.pn * BM + wc * 32 + 8 * fq;
; #pragma unroll
;         for (int ai = 0; ai < 2; ++ai)
; #pragma unroll
;             for (int m = 0; m < 4; ++m) {
;                 const int row = row0 + ai * HALF + m * 16; const size_t off = (size_t)row * 1024 + col0; float s = 0.f;
; #pragma unroll
;                 for (int bj = 0; bj < 2; ++bj) { const size_t o2 = off + bj * HALF;
;                     f32x4 b0, b1;
;                     if (BASE_F32) { b0 = *(const f32x4*)(basef + o2); b1 = *(const f32x4*)(basef + o2 + 4); }
;                     else { const u32x4 p = *(const u32x4*)(xb + o2);
;                         b0 = (f32x4){__builtin_bit_cast(float, p.x << 16), __builtin_bit_cast(float, p.x & 0xffff0000u), __builtin_bit_cast(float, p.y << 16), __builtin_bit_cast(float, p.y & 0xffff0000u)};
;                         b1 = (f32x4){__builtin_bit_cast(float, p.z << 16), __builtin_bit_cast(float, p.z & 0xffff0000u), __builtin_bit_cast(float, p.w << 16), __builtin_bit_cast(float, p.w & 0xffff0000u)}; }
;                     const f32x4 o0 = b0 + acc[ai][bj][m][0], o1 = b1 + acc[ai][bj][m][1];
;                     s += ((o0[0] * o0[0] + o0[1] * o0[1]) + (o0[2] * o0[2] + o0[3] * o0[3])) + ((o1[0] * o1[0] + o1[1] * o1[1]) + (o1[2] * o1[2] + o1[3] * o1[3]));
;                     u32x4 w; w.x = cvt_pk_bf16(o0[0], o0[1]); w.y = cvt_pk_bf16(o0[2], o0[3]); w.z = cvt_pk_bf16(o1[0], o1[1]); w.w = cvt_pk_bf16(o1[2], o1[3]);
;                     *(u32x4*)(xb + o2) = w; }
;                 s += __shfl_xor(s, 16); s += __shfl_xor(s, 32);
;                 if (fq == 0) atomicAdd(ssq + row, s);
.LBB0_2537:
	s_or_b64 exec, exec, s[22:23]
	v_add_u32_e32 v34, 0xa0, v148
	s_waitcnt lgkmcnt(0)
	v_ashrrev_i32_e32 v35, 31, v34
	v_lshlrev_b64 v[36:37], 11, v[34:35]
	v_lshl_add_u64 v[36:37], s[80:81], 0, v[36:37]
	v_lshl_add_u64 v[40:41], v[146:147], 1, v[36:37]
	global_load_dwordx4 v[36:39], v[40:41], off
	s_waitcnt vmcnt(0)
	v_lshlrev_b32_e32 v42, 16, v36
	v_and_b32_e32 v43, 0xffff0000, v36
	v_lshlrev_b32_e32 v36, 16, v37
	v_and_b32_e32 v37, 0xffff0000, v37
	v_lshlrev_b32_e32 v44, 16, v38
	v_and_b32_e32 v45, 0xffff0000, v38
	v_lshlrev_b32_e32 v38, 16, v39
	v_and_b32_e32 v39, 0xffff0000, v39
	v_pk_add_f32 v[36:37], v[32:33], v[36:37]
	v_pk_add_f32 v[42:43], v[30:31], v[42:43]
	v_pk_add_f32 v[38:39], v[28:29], v[38:39]
	v_pk_add_f32 v[44:45], v[26:27], v[44:45]
	v_cvt_pk_bf16_f32 v26, v42, v43
	v_cvt_pk_bf16_f32 v27, v36, v37
	v_mul_f32_e32 v43, v43, v43
	v_cvt_pk_bf16_f32 v28, v44, v45
	v_cvt_pk_bf16_f32 v29, v38, v39
	global_load_dwordx4 v[30:33], v[40:41], off offset:256
	v_mul_f32_e32 v37, v37, v37
	v_mul_f32_e32 v45, v45, v45
	v_mul_f32_e32 v39, v39, v39
	v_fmac_f32_e32 v43, v42, v42
	v_fmac_f32_e32 v37, v36, v36
	v_fmac_f32_e32 v45, v44, v44
	v_fmac_f32_e32 v39, v38, v38
	v_add_f32_e32 v36, v43, v37
	v_add_f32_e32 v37, v45, v39
	v_add_f32_e32 v42, v36, v37
	global_store_dwordx4 v[40:41], v[26:29], off sc0 sc1
	s_waitcnt vmcnt(1)
	v_lshlrev_b32_e32 v36, 16, v30
	v_and_b32_e32 v37, 0xffff0000, v30
	v_lshlrev_b32_e32 v30, 16, v31
	v_and_b32_e32 v31, 0xffff0000, v31
	v_lshlrev_b32_e32 v38, 16, v32
	v_and_b32_e32 v39, 0xffff0000, v32
	v_lshlrev_b32_e32 v32, 16, v33
	v_and_b32_e32 v33, 0xffff0000, v33
	v_pk_add_f32 v[24:25], v[24:25], v[30:31]
	v_pk_add_f32 v[22:23], v[22:23], v[36:37]
	v_pk_add_f32 v[30:31], v[20:21], v[32:33]
	v_pk_add_f32 v[32:33], v[18:19], v[38:39]
	v_mul_f32_e32 v18, v23, v23
	v_mul_f32_e32 v19, v25, v25
	v_mul_f32_e32 v20, v33, v33
	v_mul_f32_e32 v21, v31, v31
	v_fmac_f32_e32 v18, v22, v22
	v_fmac_f32_e32 v19, v24, v24
	v_fmac_f32_e32 v20, v32, v32
	v_fmac_f32_e32 v21, v30, v30
	v_add_f32_e32 v18, v18, v19
	v_add_f32_e32 v19, v20, v21
	v_add_f32_e32 v18, v18, v19
	v_add_f32_e32 v18, v42, v18
	ds_bpermute_b32 v19, v122, v18
	v_cvt_pk_bf16_f32 v20, v22, v23
	v_cvt_pk_bf16_f32 v21, v24, v25
	v_cvt_pk_bf16_f32 v22, v32, v33
	v_cvt_pk_bf16_f32 v23, v30, v31
	s_waitcnt lgkmcnt(0)
	v_add_f32_e32 v18, v18, v19
	ds_bpermute_b32 v19, v116, v18
	global_store_dwordx4 v[40:41], v[20:23], off offset:256 sc0 sc1
	s_and_saveexec_b64 s[22:23], s[4:5]
	s_cbranch_execz .LBB0_2539
	s_waitcnt lgkmcnt(0)
	v_add_f32_e32 v20, v18, v19
	v_lshl_add_u64 v[18:19], v[34:35], 2, s[10:11]
	global_atomic_add_f32 v[18:19], v20, off
.LBB0_2539:
	s_or_b64 exec, exec, s[22:23]
	v_add_u32_e32 v18, 0xb0, v148
	s_waitcnt lgkmcnt(0)
	v_ashrrev_i32_e32 v19, 31, v18
	v_lshlrev_b64 v[20:21], 11, v[18:19]
	v_lshl_add_u64 v[20:21], s[80:81], 0, v[20:21]
	v_lshl_add_u64 v[24:25], v[146:147], 1, v[20:21]
	global_load_dwordx4 v[20:23], v[24:25], off
	s_waitcnt vmcnt(0)
	v_lshlrev_b32_e32 v26, 16, v20
	v_and_b32_e32 v27, 0xffff0000, v20
	v_lshlrev_b32_e32 v20, 16, v21
	v_and_b32_e32 v21, 0xffff0000, v21
	v_lshlrev_b32_e32 v28, 16, v22
	v_and_b32_e32 v29, 0xffff0000, v22
	v_lshlrev_b32_e32 v22, 16, v23
	v_and_b32_e32 v23, 0xffff0000, v23
	v_pk_add_f32 v[20:21], v[16:17], v[20:21]
	v_pk_add_f32 v[26:27], v[14:15], v[26:27]
	v_pk_add_f32 v[22:23], v[12:13], v[22:23]
	v_pk_add_f32 v[28:29], v[10:11], v[28:29]
	v_cvt_pk_bf16_f32 v10, v26, v27
	v_cvt_pk_bf16_f32 v11, v20, v21
	v_mul_f32_e32 v27, v27, v27
	v_cvt_pk_bf16_f32 v12, v28, v29
	v_cvt_pk_bf16_f32 v13, v22, v23
	global_load_dwordx4 v[14:17], v[24:25], off offset:256
	v_mul_f32_e32 v21, v21, v21
	v_mul_f32_e32 v29, v29, v29
	v_mul_f32_e32 v23, v23, v23
	v_fmac_f32_e32 v27, v26, v26
	v_fmac_f32_e32 v21, v20, v20
	v_fmac_f32_e32 v29, v28, v28
	v_fmac_f32_e32 v23, v22, v22
	v_add_f32_e32 v20, v27, v21
	v_add_f32_e32 v21, v29, v23
	v_add_f32_e32 v26, v20, v21
	global_store_dwordx4 v[24:25], v[10:13], off sc0 sc1
	s_waitcnt vmcnt(1)
	v_lshlrev_b32_e32 v20, 16, v14
	v_and_b32_e32 v21, 0xffff0000, v14
	v_lshlrev_b32_e32 v14, 16, v15
	v_and_b32_e32 v15, 0xffff0000, v15
	v_lshlrev_b32_e32 v22, 16, v16
	v_and_b32_e32 v23, 0xffff0000, v16
	v_lshlrev_b32_e32 v16, 16, v17
	v_and_b32_e32 v17, 0xffff0000, v17
	v_pk_add_f32 v[8:9], v[8:9], v[14:15]
	v_pk_add_f32 v[6:7], v[6:7], v[20:21]
	v_pk_add_f32 v[14:15], v[4:5], v[16:17]
	v_pk_add_f32 v[16:17], v[2:3], v[22:23]
	v_mul_f32_e32 v2, v7, v7
	v_mul_f32_e32 v3, v9, v9
	v_mul_f32_e32 v4, v17, v17
	v_mul_f32_e32 v5, v15, v15
	v_fmac_f32_e32 v2, v6, v6
	v_fmac_f32_e32 v3, v8, v8
	v_fmac_f32_e32 v4, v16, v16
	v_fmac_f32_e32 v5, v14, v14
	v_add_f32_e32 v2, v2, v3
	v_add_f32_e32 v3, v4, v5
	v_add_f32_e32 v2, v2, v3
	v_add_f32_e32 v2, v26, v2
	ds_bpermute_b32 v3, v122, v2
	v_cvt_pk_bf16_f32 v4, v6, v7
	v_cvt_pk_bf16_f32 v5, v8, v9
	v_cvt_pk_bf16_f32 v6, v16, v17
	v_cvt_pk_bf16_f32 v7, v14, v15
	s_waitcnt lgkmcnt(0)
	v_add_f32_e32 v2, v2, v3
	ds_bpermute_b32 v3, v116, v2
	global_store_dwordx4 v[24:25], v[4:7], off offset:256 sc0 sc1
	s_and_saveexec_b64 s[22:23], s[4:5]
	s_cbranch_execz .LBB0_2541
	s_waitcnt lgkmcnt(0)
	v_add_f32_e32 v4, v2, v3
	v_lshl_add_u64 v[2:3], v[18:19], 2, s[10:11]
	global_atomic_add_f32 v[2:3], v4, off

;     __device__ __forceinline__ void operator()(const f32x4 (&acc)[2][2][4][2], const Unit& u, int wr, int wc, int fr, int fq) const {
;         typedef _Float16 f16x8 __attribute__((ext_vector_type(8)));
;         const int row0 = u.pm * BM + wr * 64 + fr, col0 = u.pn * BM + wc * 32 + 8 * fq;
; #pragma unroll
;         for (int ai = 0; ai < 2; ++ai)
; #pragma unroll
;             for (int m = 0; m < 4; ++m) {
;                 const int row = row0 + ai * HALF + m * 16;
;                 const float sc = rsqrtf(ssq[row] * (1.0f / 1024.0f) + 1e-6f);
;                 _Float16* rowp = O + (size_t)row * ld + col0;
; #pragma unroll
;                 for (int bj = 0; bj < 2; ++bj) { const f32x4 v0 = acc[ai][bj][m][0] * sc, v1 = acc[ai][bj][m][1] * sc;
;                     f16x8 w; w[0] = (_Float16)v0[0]; w[1] = (_Float16)v0[1]; w[2] = (_Float16)v0[2]; w[3] = (_Float16)v0[3];
;                     w[4] = (_Float16)v1[0]; w[5] = (_Float16)v1[1]; w[6] = (_Float16)v1[2]; w[7] = (_Float16)v1[3];
;                     *(f16x8*)(rowp + bj * HALF) = w; } }
.LBB0_2616:
	v_lshl_add_u32 v156, s0, 8, v148
	v_ashrrev_i32_e32 v157, 31, v156
	v_lshl_add_u64 v[144:145], v[156:157], 2, s[12:13]
	global_load_dword v155, v[144:145], off
	v_lshl_or_b32 v146, s1, 8, v150
	v_ashrrev_i32_e32 v147, 31, v146
	v_lshlrev_b64 v[162:163], 1, v[146:147]
	v_lshlrev_b64 v[160:161], 12, v[156:157]
	v_or_b32_e32 v158, 16, v156
	v_ashrrev_i32_e32 v159, 31, v158
	s_waitcnt vmcnt(0)
	v_fmamk_f32 v146, v155, 0x3a800000, v154
	v_mul_f32_e32 v147, 0x4b800000, v146
	v_cmp_gt_f32_e32 vcc, s57, v146
	s_nop 1
	v_cndmask_b32_e32 v146, v146, v147, vcc
	v_rsq_f32_e32 v155, v146
	v_lshl_add_u64 v[146:147], s[10:11], 0, v[160:161]
	v_lshl_add_u64 v[146:147], v[146:147], 0, v[162:163]
	v_lshl_add_u64 v[160:161], v[158:159], 2, s[12:13]
	v_mul_f32_e32 v157, 0x45800000, v155
	v_cndmask_b32_e32 v164, v155, v157, vcc
	v_pk_mul_f32 v[126:127], v[126:127], v[164:165] op_sel_hi:[1,0]
	v_pk_mul_f32 v[124:125], v[124:125], v[164:165] op_sel_hi:[1,0]
	v_pk_mul_f32 v[122:123], v[122:123], v[164:165] op_sel_hi:[1,0]
	v_pk_mul_f32 v[120:121], v[120:121], v[164:165] op_sel_hi:[1,0]
	v_pk_mul_f32 v[166:167], v[118:119], v[164:165] op_sel_hi:[1,0]
	v_pk_mul_f32 v[168:169], v[116:117], v[164:165] op_sel_hi:[1,0]
	v_pk_mul_f32 v[116:117], v[114:115], v[164:165] op_sel_hi:[1,0]
	v_pk_mul_f32 v[164:165], v[112:113], v[164:165] op_sel_hi:[1,0]
	v_cvt_pk_f16_f32 v115, v122, v123
	v_cvt_pk_f16_f32 v114, v120, v121
	v_cvt_pk_f16_f32 v113, v126, v127
	v_cvt_pk_f16_f32 v112, v124, v125
	v_cvt_pk_f16_f32 v119, v116, v117
	v_cvt_pk_f16_f32 v118, v164, v165
	v_cvt_pk_f16_f32 v117, v166, v167
	v_cvt_pk_f16_f32 v116, v168, v169
	global_store_dwordx4 v[146:147], v[112:115], off sc0 sc1
	global_store_dwordx4 v[146:147], v[116:119], off offset:256 sc0 sc1
	global_load_dword v116, v[160:161], off
	v_lshlrev_b64 v[114:115], 12, v[158:159]
	v_or_b32_e32 v112, 32, v156
	v_lshl_add_u64 v[114:115], s[10:11], 0, v[114:115]
	v_ashrrev_i32_e32 v113, 31, v112
	v_lshl_add_u64 v[114:115], v[114:115], 0, v[162:163]
	s_waitcnt vmcnt(0)
	v_fmamk_f32 v116, v116, 0x3a800000, v154
	v_mul_f32_e32 v117, 0x4b800000, v116
	v_cmp_gt_f32_e32 vcc, s57, v116
	s_nop 1
	v_cndmask_b32_e32 v116, v116, v117, vcc
	v_rsq_f32_e32 v118, v116
	v_lshl_add_u64 v[116:117], v[112:113], 2, s[12:13]
	v_mul_f32_e32 v119, 0x45800000, v118
	v_cndmask_b32_e32 v118, v118, v119, vcc
	v_pk_mul_f32 v[110:111], v[110:111], v[118:119] op_sel_hi:[1,0]
	v_pk_mul_f32 v[108:109], v[108:109], v[118:119] op_sel_hi:[1,0]
	v_pk_mul_f32 v[106:107], v[106:107], v[118:119] op_sel_hi:[1,0]
	v_pk_mul_f32 v[104:105], v[104:105], v[118:119] op_sel_hi:[1,0]
	v_pk_mul_f32 v[120:121], v[102:103], v[118:119] op_sel_hi:[1,0]
	v_pk_mul_f32 v[122:123], v[100:101], v[118:119] op_sel_hi:[1,0]
	v_pk_mul_f32 v[100:101], v[98:99], v[118:119] op_sel_hi:[1,0]
	v_pk_mul_f32 v[118:119], v[96:97], v[118:119] op_sel_hi:[1,0]
	v_cvt_pk_f16_f32 v99, v106, v107
	v_cvt_pk_f16_f32 v98, v104, v105
	v_cvt_pk_f16_f32 v97, v110, v111
	v_cvt_pk_f16_f32 v96, v108, v109
	v_cvt_pk_f16_f32 v103, v100, v101
	v_cvt_pk_f16_f32 v102, v118, v119
	v_cvt_pk_f16_f32 v101, v120, v121
	v_cvt_pk_f16_f32 v100, v122, v123
	global_store_dwordx4 v[114:115], v[96:99], off sc0 sc1
	global_store_dwordx4 v[114:115], v[100:103], off offset:256 sc0 sc1
	global_load_dword v100, v[116:117], off
	v_lshlrev_b64 v[98:99], 12, v[112:113]
	v_or_b32_e32 v96, 48, v156
	v_lshl_add_u64 v[98:99], s[10:11], 0, v[98:99]
	v_ashrrev_i32_e32 v97, 31, v96
	v_lshl_add_u64 v[98:99], v[98:99], 0, v[162:163]
	s_waitcnt vmcnt(0)
	v_fmamk_f32 v100, v100, 0x3a800000, v154
	v_mul_f32_e32 v101, 0x4b800000, v100
	v_cmp_gt_f32_e32 vcc, s57, v100
	s_nop 1
	v_cndmask_b32_e32 v100, v100, v101, vcc
	v_rsq_f32_e32 v102, v100
	v_lshl_add_u64 v[100:101], v[96:97], 2, s[12:13]
	v_mul_f32_e32 v103, 0x45800000, v102
	v_cndmask_b32_e32 v102, v102, v103, vcc
	v_pk_mul_f32 v[94:95], v[94:95], v[102:103] op_sel_hi:[1,0]
	v_pk_mul_f32 v[92:93], v[92:93], v[102:103] op_sel_hi:[1,0]
	v_pk_mul_f32 v[90:91], v[90:91], v[102:103] op_sel_hi:[1,0]
	v_pk_mul_f32 v[88:89], v[88:89], v[102:103] op_sel_hi:[1,0]
	v_pk_mul_f32 v[104:105], v[86:87], v[102:103] op_sel_hi:[1,0]
	v_pk_mul_f32 v[106:107], v[84:85], v[102:103] op_sel_hi:[1,0]
	v_pk_mul_f32 v[84:85], v[82:83], v[102:103] op_sel_hi:[1,0]
	v_pk_mul_f32 v[102:103], v[80:81], v[102:103] op_sel_hi:[1,0]
	v_cvt_pk_f16_f32 v83, v90, v91
	v_cvt_pk_f16_f32 v82, v88, v89
	v_cvt_pk_f16_f32 v81, v94, v95
	v_cvt_pk_f16_f32 v80, v92, v93
	v_cvt_pk_f16_f32 v87, v84, v85
	v_cvt_pk_f16_f32 v86, v102, v103
	v_cvt_pk_f16_f32 v85, v104, v105
	v_cvt_pk_f16_f32 v84, v106, v107
	global_store_dwordx4 v[98:99], v[80:83], off sc0 sc1
	global_store_dwordx4 v[98:99], v[84:87], off offset:256 sc0 sc1
	global_load_dword v80, v[100:101], off
	s_waitcnt vmcnt(0)
	v_fmamk_f32 v80, v80, 0x3a800000, v154
	v_mul_f32_e32 v81, 0x4b800000, v80
	v_cmp_gt_f32_e32 vcc, s57, v80
	s_nop 1
	v_cndmask_b32_e32 v80, v80, v81, vcc
	v_rsq_f32_e32 v82, v80
	v_lshlrev_b64 v[80:81], 12, v[96:97]
	v_lshl_add_u64 v[80:81], s[10:11], 0, v[80:81]
	v_lshl_add_u64 v[80:81], v[80:81], 0, v[162:163]
	v_mul_f32_e32 v83, 0x45800000, v82
	v_cndmask_b32_e32 v82, v82, v83, vcc
	v_pk_mul_f32 v[78:79], v[78:79], v[82:83] op_sel_hi:[1,0]
	v_pk_mul_f32 v[76:77], v[76:77], v[82:83] op_sel_hi:[1,0]
	v_pk_mul_f32 v[74:75], v[74:75], v[82:83] op_sel_hi:[1,0]
	v_pk_mul_f32 v[72:73], v[72:73], v[82:83] op_sel_hi:[1,0]
	v_pk_mul_f32 v[84:85], v[70:71], v[82:83] op_sel_hi:[1,0]
	v_pk_mul_f32 v[86:87], v[68:69], v[82:83] op_sel_hi:[1,0]
	v_pk_mul_f32 v[68:69], v[66:67], v[82:83] op_sel_hi:[1,0]
	v_pk_mul_f32 v[82:83], v[64:65], v[82:83] op_sel_hi:[1,0]
	v_cvt_pk_f16_f32 v67, v74, v75
	v_cvt_pk_f16_f32 v66, v72, v73
	v_cvt_pk_f16_f32 v65, v78, v79
	v_cvt_pk_f16_f32 v64, v76, v77
	v_cvt_pk_f16_f32 v71, v68, v69
	v_cvt_pk_f16_f32 v70, v82, v83
	v_cvt_pk_f16_f32 v69, v84, v85
	v_cvt_pk_f16_f32 v68, v86, v87
	global_store_dwordx4 v[80:81], v[64:67], off sc0 sc1
	global_store_dwordx4 v[80:81], v[68:71], off offset:256 sc0 sc1
	global_load_dword v66, v[144:145], off offset:512
	v_lshl_add_u64 v[64:65], v[146:147], 0, s[18:19]
	s_waitcnt vmcnt(0)
; #define PG8_BAR __builtin_amdgcn_s_barrier()
; template <class Epi, class Sched, bool ALIGN_EPI = false, bool SP2 = false>
; __device__ __forceinline__ void gemm_phase(PG8_LAS unsigned char* lds, const Gemm g, const Sched& S, const Epi& E) {
;     ...
;         if constexpr (ALIGN_EPI) { if (wr == 0) PG8_BAR; }
;         if constexpr (!Epi::AFTER_DRAIN) { E(acc, cur, wr, wc, fr, fq); S.done(cur); }
;         if (!has_next) break;
; #pragma unroll
;         for (int a = 0; a < 2; ++a)
; #pragma unroll
;             for (int b = 0; b < 2; ++b)
; #pragma unroll
;                 for (int m = 0; m < 4; ++m)
; #pragma unroll
;                     for (int n = 0; n < 2; ++n) acc[a][b][m][n] = (f32x4){0.f, 0.f, 0.f, 0.f};
;         cur = nxt; cA = nA; cB = nB; ++ui;
;         if constexpr (ALIGN_EPI) { if (wr == 1) PG8_BAR; }
;     __device__ __forceinline__ void operator()(const f32x4 (&acc)[2][2][4][2], const Unit& u, int wr, int wc, int fr, int fq) const {
;         typedef _Float16 f16x8 __attribute__((ext_vector_type(8)));
;         const int row0 = u.pm * BM + wr * 64 + fr, col0 = u.pn * BM + wc * 32 + 8 * fq;
; #pragma unroll
;         for (int ai = 0; ai < 2; ++ai)
; #pragma unroll
;             for (int m = 0; m < 4; ++m) {
;                 const int row = row0 + ai * HALF + m * 16;
;                 const float sc = rsqrtf(ssq[row] * (1.0f / 1024.0f) + 1e-6f);
;                 _Float16* rowp = O + (size_t)row * ld + col0;
; #pragma unroll
;                 for (int bj = 0; bj < 2; ++bj) { const f32x4 v0 = acc[ai][bj][m][0] * sc, v1 = acc[ai][bj][m][1] * sc;
;                     f16x8 w; w[0] = (_Float16)v0[0]; w[1] = (_Float16)v0[1]; w[2] = (_Float16)v0[2]; w[3] = (_Float16)v0[3];
;                     w[4] = (_Float16)v1[0]; w[5] = (_Float16)v1[1]; w[6] = (_Float16)v1[2]; w[7] = (_Float16)v1[3];
;                     *(f16x8*)(rowp + bj * HALF) = w; } }
	v_fmamk_f32 v66, v66, 0x3a800000, v154
	v_mul_f32_e32 v67, 0x4b800000, v66
	v_cmp_gt_f32_e32 vcc, s57, v66
	s_nop 1
	v_cndmask_b32_e32 v66, v66, v67, vcc
	v_rsq_f32_e32 v68, v66
	v_add_co_u32_e64 v66, s[0:1], s58, v146
	v_mul_f32_e32 v69, 0x45800000, v68
	v_cndmask_b32_e32 v68, v68, v69, vcc
	v_pk_mul_f32 v[62:63], v[62:63], v[68:69] op_sel_hi:[1,0]
	v_pk_mul_f32 v[60:61], v[60:61], v[68:69] op_sel_hi:[1,0]
	v_pk_mul_f32 v[58:59], v[58:59], v[68:69] op_sel_hi:[1,0]
	v_pk_mul_f32 v[56:57], v[56:57], v[68:69] op_sel_hi:[1,0]
	v_addc_co_u32_e64 v67, s[0:1], 0, v147, s[0:1]
	v_pk_mul_f32 v[70:71], v[54:55], v[68:69] op_sel_hi:[1,0]
	v_pk_mul_f32 v[72:73], v[52:53], v[68:69] op_sel_hi:[1,0]
	v_pk_mul_f32 v[52:53], v[50:51], v[68:69] op_sel_hi:[1,0]
	v_pk_mul_f32 v[68:69], v[48:49], v[68:69] op_sel_hi:[1,0]
	v_cvt_pk_f16_f32 v51, v58, v59
	v_cvt_pk_f16_f32 v50, v56, v57
	v_cvt_pk_f16_f32 v49, v62, v63
	v_cvt_pk_f16_f32 v48, v60, v61
	v_cvt_pk_f16_f32 v55, v52, v53
	v_cvt_pk_f16_f32 v54, v68, v69
	v_cvt_pk_f16_f32 v53, v70, v71
	v_cvt_pk_f16_f32 v52, v72, v73
	global_store_dwordx4 v[66:67], v[48:51], off sc0 sc1
	global_store_dwordx4 v[64:65], v[52:55], off offset:256 sc0 sc1
	global_load_dword v50, v[144:145], off offset:576
	v_lshl_add_u64 v[48:49], v[146:147], 0, s[20:21]
	s_waitcnt vmcnt(0)
	v_fmamk_f32 v50, v50, 0x3a800000, v154
	v_mul_f32_e32 v51, 0x4b800000, v50
	v_cmp_gt_f32_e32 vcc, s57, v50
	s_nop 1
	v_cndmask_b32_e32 v50, v50, v51, vcc
	v_rsq_f32_e32 v52, v50
	v_add_co_u32_e64 v50, s[0:1], s59, v146
	v_mul_f32_e32 v53, 0x45800000, v52
	v_cndmask_b32_e32 v52, v52, v53, vcc
	v_pk_mul_f32 v[46:47], v[46:47], v[52:53] op_sel_hi:[1,0]
	v_pk_mul_f32 v[44:45], v[44:45], v[52:53] op_sel_hi:[1,0]
	v_pk_mul_f32 v[42:43], v[42:43], v[52:53] op_sel_hi:[1,0]
	v_pk_mul_f32 v[40:41], v[40:41], v[52:53] op_sel_hi:[1,0]
	v_addc_co_u32_e64 v51, s[0:1], 0, v147, s[0:1]
	v_pk_mul_f32 v[54:55], v[38:39], v[52:53] op_sel_hi:[1,0]
	v_pk_mul_f32 v[56:57], v[36:37], v[52:53] op_sel_hi:[1,0]
	v_pk_mul_f32 v[36:37], v[34:35], v[52:53] op_sel_hi:[1,0]
	v_pk_mul_f32 v[52:53], v[32:33], v[52:53] op_sel_hi:[1,0]
	v_cvt_pk_f16_f32 v35, v42, v43
	v_cvt_pk_f16_f32 v34, v40, v41
	v_cvt_pk_f16_f32 v33, v46, v47
	v_cvt_pk_f16_f32 v32, v44, v45
	v_cvt_pk_f16_f32 v39, v36, v37
	v_cvt_pk_f16_f32 v38, v52, v53
	v_cvt_pk_f16_f32 v37, v54, v55
	v_cvt_pk_f16_f32 v36, v56, v57
	global_store_dwordx4 v[50:51], v[32:35], off sc0 sc1
	global_store_dwordx4 v[48:49], v[36:39], off offset:256 sc0 sc1
	global_load_dword v34, v[144:145], off offset:640
	v_lshl_add_u64 v[32:33], v[146:147], 0, s[36:37]
	s_waitcnt vmcnt(0)
	v_fmamk_f32 v34, v34, 0x3a800000, v154
	v_mul_f32_e32 v35, 0x4b800000, v34
	v_cmp_gt_f32_e32 vcc, s57, v34
	s_nop 1
	v_cndmask_b32_e32 v34, v34, v35, vcc
	v_rsq_f32_e32 v36, v34
	v_add_co_u32_e64 v34, s[0:1], s60, v146
	v_mul_f32_e32 v37, 0x45800000, v36
	v_cndmask_b32_e32 v36, v36, v37, vcc
	v_pk_mul_f32 v[30:31], v[30:31], v[36:37] op_sel_hi:[1,0]
	v_pk_mul_f32 v[28:29], v[28:29], v[36:37] op_sel_hi:[1,0]
	v_pk_mul_f32 v[26:27], v[26:27], v[36:37] op_sel_hi:[1,0]
	v_pk_mul_f32 v[24:25], v[24:25], v[36:37] op_sel_hi:[1,0]
	v_addc_co_u32_e64 v35, s[0:1], 0, v147, s[0:1]
	v_pk_mul_f32 v[38:39], v[22:23], v[36:37] op_sel_hi:[1,0]
	v_pk_mul_f32 v[40:41], v[20:21], v[36:37] op_sel_hi:[1,0]
	v_pk_mul_f32 v[20:21], v[18:19], v[36:37] op_sel_hi:[1,0]
	v_pk_mul_f32 v[36:37], v[16:17], v[36:37] op_sel_hi:[1,0]
	v_cvt_pk_f16_f32 v19, v26, v27
	v_cvt_pk_f16_f32 v18, v24, v25
	v_cvt_pk_f16_f32 v17, v30, v31
	v_cvt_pk_f16_f32 v16, v28, v29
	v_cvt_pk_f16_f32 v23, v20, v21
	v_cvt_pk_f16_f32 v22, v36, v37
	v_cvt_pk_f16_f32 v21, v38, v39
	v_cvt_pk_f16_f32 v20, v40, v41
	global_store_dwordx4 v[34:35], v[16:19], off sc0 sc1
	global_store_dwordx4 v[32:33], v[20:23], off offset:256 sc0 sc1
	global_load_dword v18, v[144:145], off offset:704
	s_andn2_b64 vcc, exec, s[4:5]
	v_lshl_add_u64 v[16:17], v[146:147], 0, s[38:39]
	s_waitcnt vmcnt(0)
	v_fmamk_f32 v18, v18, 0x3a800000, v154
	v_mul_f32_e32 v19, 0x4b800000, v18
	v_cmp_gt_f32_e64 s[0:1], s57, v18
	s_nop 1
	v_cndmask_b32_e64 v18, v18, v19, s[0:1]
	v_rsq_f32_e32 v20, v18
	v_add_co_u32_e64 v18, s[4:5], s61, v146
	v_mul_f32_e32 v21, 0x45800000, v20
	v_cndmask_b32_e64 v20, v20, v21, s[0:1]
	v_pk_mul_f32 v[14:15], v[14:15], v[20:21] op_sel_hi:[1,0]
	v_pk_mul_f32 v[12:13], v[12:13], v[20:21] op_sel_hi:[1,0]
	v_pk_mul_f32 v[10:11], v[10:11], v[20:21] op_sel_hi:[1,0]
	v_pk_mul_f32 v[8:9], v[8:9], v[20:21] op_sel_hi:[1,0]
	v_addc_co_u32_e64 v19, s[4:5], 0, v147, s[4:5]
	v_pk_mul_f32 v[22:23], v[6:7], v[20:21] op_sel_hi:[1,0]
	v_pk_mul_f32 v[24:25], v[4:5], v[20:21] op_sel_hi:[1,0]
	v_pk_mul_f32 v[4:5], v[2:3], v[20:21] op_sel_hi:[1,0]
	v_pk_mul_f32 v[20:21], v[0:1], v[20:21] op_sel_hi:[1,0]
	v_cvt_pk_f16_f32 v3, v10, v11
	v_cvt_pk_f16_f32 v2, v8, v9
	v_cvt_pk_f16_f32 v1, v14, v15
	v_cvt_pk_f16_f32 v0, v12, v13
	s_mov_b64 s[0:1], -1
	v_cvt_pk_f16_f32 v7, v4, v5
	v_cvt_pk_f16_f32 v6, v20, v21
	v_cvt_pk_f16_f32 v5, v22, v23
	v_cvt_pk_f16_f32 v4, v24, v25
	global_store_dwordx4 v[18:19], v[0:3], off sc0 sc1
	global_store_dwordx4 v[16:17], v[4:7], off offset:256 sc0 sc1
	s_cbranch_vccnz .LBB0_2605
	s_andn2_b64 vcc, exec, s[8:9]
	s_cbranch_vccnz .LBB0_2604
	s_barrier
	s_branch .LBB0_2604
